# v43 with the in-loop s_setprio flips and the redundant post-barrier lgkmcnt(0) waits deleted from the five GEMM K-loops
# speedup vs baseline: 1.0048x; 1.0048x over previous
; #define PG8_STAGE(bufoff, gbase, voff) do { _Pragma("unroll") for (int _i = 0; _i < 2; ++_i) \
;         __builtin_amdgcn_global_load_lds((const unsigned*)((const char*)(gbase) + (voff)[_i]), (PG8_LAS unsigned*)(lds + (bufoff) + ldsw + _i * 8192), 16, 0, 0); } while (0)
; #define PG8_LDA(dst, b, h) do { _Pragma("unroll") for (int m = 0; m < 4; ++m) _Pragma("unroll") for (int k = 0; k < 2; ++k) dst[m][k] = *(const PG8_LAS bf16x8*)(lds + PG8_SA(b, h) + aoff + m * 2048 + k * 1024); } while (0)
; #define PG8_LDB(dst, b, h) do { _Pragma("unroll") for (int n = 0; n < 2; ++n) _Pragma("unroll") for (int k = 0; k < 2; ++k) dst[n][k] = *(const PG8_LAS bf16x8*)(lds + PG8_SB(b, h) + boff + n * 2048 + k * 1024); } while (0)
; #define PG8_MMA(ai, bj, At, Bt) do { __builtin_amdgcn_s_setprio(1); _Pragma("unroll") for (int m = 0; m < 4; ++m) _Pragma("unroll") for (int n = 0; n < 2; ++n) _Pragma("unroll") for (int k = 0; k < 2; ++k) \
;         acc[ai][bj][m][n] = __builtin_amdgcn_mfma_f32_16x16x32_bf16(Bt[n][k], At[m][k], acc[ai][bj][m][n], 0, 0, 0); __builtin_amdgcn_s_setprio(0); } while (0)
; #define PG8_WAIT_V(n) asm volatile("s_waitcnt vmcnt(" #n ")" ::: "memory")
; #define PG8_WAIT_L(n) asm volatile("s_waitcnt lgkmcnt(" #n ")" ::: "memory")
; #define PG8_BAR __builtin_amdgcn_s_barrier()
; #define PG8_SCHED __builtin_amdgcn_sched_barrier(0)
; template <class Epi, class Sched, bool ALIGN_EPI = false, bool SP2 = false>
; __device__ __forceinline__ void gemm_phase(PG8_LAS unsigned char* lds, const Gemm g, const Sched& S, const Epi& E) {
;     ...
;             PG8_LDB(B0, 0, 0); PG8_LDB(B1, 0, 1); PG8_SCHED; PG8_LDA(At, 0, 0); PG8_STAGE(PG8_SA(1, 1), a1 + hstep, voffA);
;     ...
;             if (PROBE_KIND == 18 && t == 0 && ui > 0 && g.probe) { const unsigned long long tq_ = __builtin_amdgcn_s_memrealtime(); PG8_WAIT_V(8); pg8_probe_acc += (unsigned)(__builtin_amdgcn_s_memrealtime() - tq_); }
;     ...
;             PG8_WAIT_V(8); PG8_WAIT_L(0); PG8_BAR; PG8_MMA(0, 0, At, B0); PG8_MMA(0, 1, At, B1); PG8_BAR; PG8_SCHED;
;             PG8_LDA(At, 0, 1); PG8_STAGE(PG8_SB(0, 0), b2, voffB); PG8_STAGE(PG8_SB(0, 1), b2 + hstep, voffB); PG8_STAGE(PG8_SA(0, 0), a2, voffA);
;             PG8_WAIT_V(8); PG8_WAIT_L(0); PG8_BAR; if (cur.half == 0) { PG8_MMA(1, 0, At, B0); PG8_MMA(1, 1, At, B1); } PG8_BAR; PG8_SCHED;
.LBB0_395:
	s_add_u32 s0, s8, 0xfffc0080
	s_addc_u32 s1, s9, -1
	s_add_i32 s61, 0, 0x10000
	s_cmp_eq_u32 s39, 12
	s_cselect_b32 s11, s12, s1
	s_cselect_b32 s10, s13, s0
	v_add_u32_e32 v2, s61, v203
	s_cselect_b32 s1, s14, s38
	s_cselect_b32 s0, s15, s36
	s_add_i32 s63, 0, 0x14000
	ds_read_b128 v[132:135], v2
	ds_read_b128 v[136:139], v2 offset:1024
	ds_read_b128 v[140:143], v2 offset:2048
	ds_read_b128 v[144:147], v2 offset:3072
	v_add_u32_e32 v2, s63, v203
	ds_read_b128 v[148:151], v2
	ds_read_b128 v[152:155], v2 offset:1024
	ds_read_b128 v[156:159], v2 offset:2048
	ds_read_b128 v[160:163], v2 offset:3072
	v_lshl_add_u64 v[228:229], s[8:9], 0, v[178:179]
	s_add_i32 m0, s19, 0xc000
	ds_read_b128 v[182:185], v206
	ds_read_b128 v[186:189], v206 offset:1024
	ds_read_b128 v[190:193], v206 offset:2048
	ds_read_b128 v[194:197], v206 offset:3072
	ds_read_b128 v[198:201], v206 offset:4096
	ds_read_b128 v[208:211], v206 offset:5120
	ds_read_b128 v[212:215], v206 offset:6144
	ds_read_b128 v[216:219], v206 offset:7168
	global_load_lds_dwordx4 v[228:229], off
	v_lshl_add_u64 v[228:229], s[8:9], 0, v[180:181]
	s_add_i32 m0, s19, 0xe000
	s_nop 0
	global_load_lds_dwordx4 v[228:229], off
	s_waitcnt vmcnt(8)
	s_waitcnt lgkmcnt(0)
	s_barrier
	v_mfma_f32_16x16x32_bf16 v[128:131], v[132:135], v[182:185], v[128:131]
	v_mfma_f32_16x16x32_bf16 v[124:127], v[140:143], v[182:185], v[124:127]
	v_mfma_f32_16x16x32_bf16 v[112:115], v[132:135], v[190:193], v[112:115]
	v_mfma_f32_16x16x32_bf16 v[108:111], v[140:143], v[190:193], v[108:111]
	v_mfma_f32_16x16x32_bf16 v[96:99], v[132:135], v[198:201], v[96:99]
	v_mfma_f32_16x16x32_bf16 v[92:95], v[140:143], v[198:201], v[92:95]
	v_mfma_f32_16x16x32_bf16 v[80:83], v[132:135], v[212:215], v[80:83]
	v_mfma_f32_16x16x32_bf16 v[76:79], v[140:143], v[212:215], v[76:79]
	v_mfma_f32_16x16x32_bf16 v[128:131], v[136:139], v[186:189], v[128:131]
	v_mfma_f32_16x16x32_bf16 v[124:127], v[144:147], v[186:189], v[124:127]
	v_mfma_f32_16x16x32_bf16 v[112:115], v[136:139], v[194:197], v[112:115]
	v_mfma_f32_16x16x32_bf16 v[108:111], v[144:147], v[194:197], v[108:111]
	v_mfma_f32_16x16x32_bf16 v[96:99], v[136:139], v[208:211], v[96:99]
	v_mfma_f32_16x16x32_bf16 v[92:95], v[144:147], v[208:211], v[92:95]
	v_mfma_f32_16x16x32_bf16 v[80:83], v[136:139], v[216:219], v[80:83]
	v_mfma_f32_16x16x32_bf16 v[76:79], v[144:147], v[216:219], v[76:79]
	v_mfma_f32_16x16x32_bf16 v[120:123], v[148:151], v[182:185], v[120:123]
	v_mfma_f32_16x16x32_bf16 v[116:119], v[156:159], v[182:185], v[116:119]
	v_mfma_f32_16x16x32_bf16 v[104:107], v[148:151], v[190:193], v[104:107]
	v_mfma_f32_16x16x32_bf16 v[100:103], v[156:159], v[190:193], v[100:103]
	v_mfma_f32_16x16x32_bf16 v[88:91], v[148:151], v[198:201], v[88:91]
	v_mfma_f32_16x16x32_bf16 v[84:87], v[156:159], v[198:201], v[84:87]
	v_mfma_f32_16x16x32_bf16 v[72:75], v[148:151], v[212:215], v[72:75]
	v_mfma_f32_16x16x32_bf16 v[68:71], v[156:159], v[212:215], v[68:71]
	v_mfma_f32_16x16x32_bf16 v[120:123], v[152:155], v[186:189], v[120:123]
	v_mfma_f32_16x16x32_bf16 v[116:119], v[160:163], v[186:189], v[116:119]
	v_mfma_f32_16x16x32_bf16 v[104:107], v[152:155], v[194:197], v[104:107]
	v_mfma_f32_16x16x32_bf16 v[100:103], v[160:163], v[194:197], v[100:103]
	v_mfma_f32_16x16x32_bf16 v[88:91], v[152:155], v[208:211], v[88:91]
	v_mfma_f32_16x16x32_bf16 v[84:87], v[160:163], v[208:211], v[84:87]
	v_mfma_f32_16x16x32_bf16 v[72:75], v[152:155], v[216:219], v[72:75]
	v_mfma_f32_16x16x32_bf16 v[68:71], v[160:163], v[216:219], v[68:71]
	s_barrier
	s_add_i32 s61, s61, s27
	v_lshl_add_u64 v[228:229], s[0:1], 0, v[166:167]
	s_mov_b32 m0, s61
	ds_read_b128 v[182:185], v206 offset:16384
	ds_read_b128 v[186:189], v206 offset:17408
	ds_read_b128 v[190:193], v206 offset:18432
	ds_read_b128 v[194:197], v206 offset:19456
	ds_read_b128 v[198:201], v206 offset:20480
	ds_read_b128 v[208:211], v206 offset:21504
	ds_read_b128 v[212:215], v206 offset:22528
	ds_read_b128 v[216:219], v206 offset:23552
	global_load_lds_dwordx4 v[228:229], off
	s_add_i32 m0, s61, 0x2000
	s_add_u32 s78, s0, 0x40000
	v_lshl_add_u64 v[230:231], s[0:1], 0, v[170:171]
	s_addc_u32 s79, s1, 0
	s_add_i32 s61, s63, s27
	global_load_lds_dwordx4 v[230:231], off
	v_lshl_add_u64 v[232:233], s[78:79], 0, v[166:167]
	s_mov_b32 m0, s61
	v_lshl_add_u64 v[234:235], s[10:11], 0, v[168:169]
	global_load_lds_dwordx4 v[232:233], off
	v_lshl_add_u64 v[232:233], s[78:79], 0, v[170:171]
	s_add_i32 m0, s61, 0x2000
	s_nop 0
	global_load_lds_dwordx4 v[232:233], off
	v_lshl_add_u64 v[232:233], s[10:11], 0, v[164:165]
	s_mov_b32 m0, s19
	s_nop 0
	global_load_lds_dwordx4 v[232:233], off
	s_mov_b32 m0, s30
	s_nop 0
	global_load_lds_dwordx4 v[234:235], off
	s_waitcnt vmcnt(8)
	s_waitcnt lgkmcnt(0)
	s_barrier
; #define PG8_STAGE(bufoff, gbase, voff) do { _Pragma("unroll") for (int _i = 0; _i < 2; ++_i) \
;         __builtin_amdgcn_global_load_lds((const unsigned*)((const char*)(gbase) + (voff)[_i]), (PG8_LAS unsigned*)(lds + (bufoff) + ldsw + _i * 8192), 16, 0, 0); } while (0)
; #define PG8_LDA(dst, b, h) do { _Pragma("unroll") for (int m = 0; m < 4; ++m) _Pragma("unroll") for (int k = 0; k < 2; ++k) dst[m][k] = *(const PG8_LAS bf16x8*)(lds + PG8_SA(b, h) + aoff + m * 2048 + k * 1024); } while (0)
; #define PG8_LDB(dst, b, h) do { _Pragma("unroll") for (int n = 0; n < 2; ++n) _Pragma("unroll") for (int k = 0; k < 2; ++k) dst[n][k] = *(const PG8_LAS bf16x8*)(lds + PG8_SB(b, h) + boff + n * 2048 + k * 1024); } while (0)
; #define PG8_MMA(ai, bj, At, Bt) do { __builtin_amdgcn_s_setprio(1); _Pragma("unroll") for (int m = 0; m < 4; ++m) _Pragma("unroll") for (int n = 0; n < 2; ++n) _Pragma("unroll") for (int k = 0; k < 2; ++k) \
;         acc[ai][bj][m][n] = __builtin_amdgcn_mfma_f32_16x16x32_bf16(Bt[n][k], At[m][k], acc[ai][bj][m][n], 0, 0, 0); __builtin_amdgcn_s_setprio(0); } while (0)
; #define PG8_WAIT_V(n) asm volatile("s_waitcnt vmcnt(" #n ")" ::: "memory")
; #define PG8_WAIT_L(n) asm volatile("s_waitcnt lgkmcnt(" #n ")" ::: "memory")
; #define PG8_BAR __builtin_amdgcn_s_barrier()
; #define PG8_SCHED __builtin_amdgcn_sched_barrier(0)
; template <class Epi, class Sched, bool ALIGN_EPI = false, bool SP2 = false>
; __device__ __forceinline__ void gemm_phase(PG8_LAS unsigned char* lds, const Gemm g, const Sched& S, const Epi& E) {
;     ...
;             PG8_WAIT_V(8); PG8_WAIT_L(0); PG8_BAR; if (cur.half == 0) { PG8_MMA(1, 0, At, B0); PG8_MMA(1, 1, At, B1); } PG8_BAR; PG8_SCHED;
;             PG8_LDB(B0, 1, 0); PG8_LDB(B1, 1, 1); PG8_SCHED; PG8_LDA(At, 1, 0); PG8_STAGE(PG8_SA(0, 1), a2 + hstep, voffA);
;             PG8_WAIT_V(8); PG8_WAIT_L(0); PG8_BAR; PG8_MMA(0, 0, At, B0); PG8_MMA(0, 1, At, B1); PG8_BAR; PG8_SCHED;
;             PG8_LDA(At, 1, 1); PG8_STAGE(PG8_SB(1, 0), b3, voffB); PG8_STAGE(PG8_SB(1, 1), b3 + hstep, voffB); PG8_STAGE(PG8_SA(1, 0), a3, voffA);
;             PG8_WAIT_V(8); PG8_WAIT_L(0); PG8_BAR; if (cur.half == 0) { PG8_MMA(1, 0, At, B0); PG8_MMA(1, 1, At, B1); } PG8_BAR; PG8_SCHED;
	v_mfma_f32_16x16x32_bf16 v[64:67], v[132:135], v[182:185], v[64:67]
	v_mfma_f32_16x16x32_bf16 v[60:63], v[140:143], v[182:185], v[60:63]
	v_mfma_f32_16x16x32_bf16 v[48:51], v[132:135], v[190:193], v[48:51]
	v_mfma_f32_16x16x32_bf16 v[44:47], v[140:143], v[190:193], v[44:47]
	v_mfma_f32_16x16x32_bf16 v[32:35], v[132:135], v[198:201], v[32:35]
	v_mfma_f32_16x16x32_bf16 v[28:31], v[140:143], v[198:201], v[28:31]
	v_mfma_f32_16x16x32_bf16 v[16:19], v[132:135], v[212:215], v[16:19]
	v_mfma_f32_16x16x32_bf16 v[12:15], v[140:143], v[212:215], v[12:15]
	v_mfma_f32_16x16x32_bf16 v[64:67], v[136:139], v[186:189], v[64:67]
	v_mfma_f32_16x16x32_bf16 v[60:63], v[144:147], v[186:189], v[60:63]
	v_mfma_f32_16x16x32_bf16 v[48:51], v[136:139], v[194:197], v[48:51]
	v_mfma_f32_16x16x32_bf16 v[44:47], v[144:147], v[194:197], v[44:47]
	v_mfma_f32_16x16x32_bf16 v[32:35], v[136:139], v[208:211], v[32:35]
	v_mfma_f32_16x16x32_bf16 v[28:31], v[144:147], v[208:211], v[28:31]
	v_mfma_f32_16x16x32_bf16 v[16:19], v[136:139], v[216:219], v[16:19]
	v_mfma_f32_16x16x32_bf16 v[12:15], v[144:147], v[216:219], v[12:15]
	v_mfma_f32_16x16x32_bf16 v[56:59], v[148:151], v[182:185], v[56:59]
	v_mfma_f32_16x16x32_bf16 v[52:55], v[156:159], v[182:185], v[52:55]
	v_mfma_f32_16x16x32_bf16 v[40:43], v[148:151], v[190:193], v[40:43]
	v_mfma_f32_16x16x32_bf16 v[36:39], v[156:159], v[190:193], v[36:39]
	v_mfma_f32_16x16x32_bf16 v[24:27], v[148:151], v[198:201], v[24:27]
	v_mfma_f32_16x16x32_bf16 v[20:23], v[156:159], v[198:201], v[20:23]
	v_mfma_f32_16x16x32_bf16 v[8:11], v[148:151], v[212:215], v[8:11]
	v_mfma_f32_16x16x32_bf16 v[4:7], v[156:159], v[212:215], v[4:7]
	v_mfma_f32_16x16x32_bf16 v[56:59], v[152:155], v[186:189], v[56:59]
	v_mfma_f32_16x16x32_bf16 v[52:55], v[160:163], v[186:189], v[52:55]
	v_mfma_f32_16x16x32_bf16 v[40:43], v[152:155], v[194:197], v[40:43]
	v_mfma_f32_16x16x32_bf16 v[36:39], v[160:163], v[194:197], v[36:39]
	v_mfma_f32_16x16x32_bf16 v[24:27], v[152:155], v[208:211], v[24:27]
	v_mfma_f32_16x16x32_bf16 v[20:23], v[160:163], v[208:211], v[20:23]
	v_mfma_f32_16x16x32_bf16 v[8:11], v[152:155], v[216:219], v[8:11]
	v_mfma_f32_16x16x32_bf16 v[4:7], v[160:163], v[216:219], v[4:7]
	s_barrier
	s_add_i32 s61, 0, 0x18000
	v_add_u32_e32 v2, s61, v203
	s_add_i32 s63, 0, 0x1c000
	ds_read_b128 v[132:135], v2
	ds_read_b128 v[136:139], v2 offset:1024
	ds_read_b128 v[140:143], v2 offset:2048
	ds_read_b128 v[144:147], v2 offset:3072
	v_add_u32_e32 v2, s63, v203
	ds_read_b128 v[148:151], v2
	ds_read_b128 v[152:155], v2 offset:1024
	ds_read_b128 v[156:159], v2 offset:2048
	ds_read_b128 v[160:163], v2 offset:3072
	s_add_u32 s10, s10, 0x40000
	s_addc_u32 s11, s11, 0
	s_mov_b32 m0, s31
	v_lshl_add_u64 v[236:237], s[10:11], 0, v[164:165]
	ds_read_b128 v[182:185], v206 offset:32768
	ds_read_b128 v[186:189], v206 offset:33792
	ds_read_b128 v[190:193], v206 offset:34816
	ds_read_b128 v[194:197], v206 offset:35840
	ds_read_b128 v[198:201], v206 offset:36864
	ds_read_b128 v[208:211], v206 offset:37888
	ds_read_b128 v[212:215], v206 offset:38912
	ds_read_b128 v[216:219], v206 offset:39936
	global_load_lds_dwordx4 v[236:237], off
	v_lshl_add_u64 v[236:237], s[10:11], 0, v[168:169]
	s_mov_b32 m0, s34
	s_nop 0
	global_load_lds_dwordx4 v[236:237], off
	s_waitcnt vmcnt(8)
	s_waitcnt lgkmcnt(0)
	s_barrier
	v_mfma_f32_16x16x32_bf16 v[128:131], v[132:135], v[182:185], v[128:131]
	v_mfma_f32_16x16x32_bf16 v[124:127], v[140:143], v[182:185], v[124:127]
	v_mfma_f32_16x16x32_bf16 v[112:115], v[132:135], v[190:193], v[112:115]
	v_mfma_f32_16x16x32_bf16 v[108:111], v[140:143], v[190:193], v[108:111]
	v_mfma_f32_16x16x32_bf16 v[96:99], v[132:135], v[198:201], v[96:99]
	v_mfma_f32_16x16x32_bf16 v[92:95], v[140:143], v[198:201], v[92:95]
	v_mfma_f32_16x16x32_bf16 v[80:83], v[132:135], v[212:215], v[80:83]
	v_mfma_f32_16x16x32_bf16 v[76:79], v[140:143], v[212:215], v[76:79]
	v_mfma_f32_16x16x32_bf16 v[128:131], v[136:139], v[186:189], v[128:131]
	v_mfma_f32_16x16x32_bf16 v[124:127], v[144:147], v[186:189], v[124:127]
	v_mfma_f32_16x16x32_bf16 v[112:115], v[136:139], v[194:197], v[112:115]
	v_mfma_f32_16x16x32_bf16 v[108:111], v[144:147], v[194:197], v[108:111]
	v_mfma_f32_16x16x32_bf16 v[96:99], v[136:139], v[208:211], v[96:99]
	v_mfma_f32_16x16x32_bf16 v[92:95], v[144:147], v[208:211], v[92:95]
	v_mfma_f32_16x16x32_bf16 v[80:83], v[136:139], v[216:219], v[80:83]
	v_mfma_f32_16x16x32_bf16 v[76:79], v[144:147], v[216:219], v[76:79]
	v_mfma_f32_16x16x32_bf16 v[120:123], v[148:151], v[182:185], v[120:123]
	v_mfma_f32_16x16x32_bf16 v[116:119], v[156:159], v[182:185], v[116:119]
	v_mfma_f32_16x16x32_bf16 v[104:107], v[148:151], v[190:193], v[104:107]
	v_mfma_f32_16x16x32_bf16 v[100:103], v[156:159], v[190:193], v[100:103]
	v_mfma_f32_16x16x32_bf16 v[88:91], v[148:151], v[198:201], v[88:91]
	v_mfma_f32_16x16x32_bf16 v[84:87], v[156:159], v[198:201], v[84:87]
	v_mfma_f32_16x16x32_bf16 v[72:75], v[148:151], v[212:215], v[72:75]
	v_mfma_f32_16x16x32_bf16 v[68:71], v[156:159], v[212:215], v[68:71]
	v_mfma_f32_16x16x32_bf16 v[120:123], v[152:155], v[186:189], v[120:123]
	v_mfma_f32_16x16x32_bf16 v[116:119], v[160:163], v[186:189], v[116:119]
	v_mfma_f32_16x16x32_bf16 v[104:107], v[152:155], v[194:197], v[104:107]
	v_mfma_f32_16x16x32_bf16 v[100:103], v[160:163], v[194:197], v[100:103]
	v_mfma_f32_16x16x32_bf16 v[88:91], v[152:155], v[208:211], v[88:91]
	v_mfma_f32_16x16x32_bf16 v[84:87], v[160:163], v[208:211], v[84:87]
	v_mfma_f32_16x16x32_bf16 v[72:75], v[152:155], v[216:219], v[72:75]
	v_mfma_f32_16x16x32_bf16 v[68:71], v[160:163], v[216:219], v[68:71]
	s_barrier
; #define PG8_STAGE(bufoff, gbase, voff) do { _Pragma("unroll") for (int _i = 0; _i < 2; ++_i) \
;         __builtin_amdgcn_global_load_lds((const unsigned*)((const char*)(gbase) + (voff)[_i]), (PG8_LAS unsigned*)(lds + (bufoff) + ldsw + _i * 8192), 16, 0, 0); } while (0)
; #define PG8_LDA(dst, b, h) do { _Pragma("unroll") for (int m = 0; m < 4; ++m) _Pragma("unroll") for (int k = 0; k < 2; ++k) dst[m][k] = *(const PG8_LAS bf16x8*)(lds + PG8_SA(b, h) + aoff + m * 2048 + k * 1024); } while (0)
; #define PG8_MMA(ai, bj, At, Bt) do { __builtin_amdgcn_s_setprio(1); _Pragma("unroll") for (int m = 0; m < 4; ++m) _Pragma("unroll") for (int n = 0; n < 2; ++n) _Pragma("unroll") for (int k = 0; k < 2; ++k) \
;         acc[ai][bj][m][n] = __builtin_amdgcn_mfma_f32_16x16x32_bf16(Bt[n][k], At[m][k], acc[ai][bj][m][n], 0, 0, 0); __builtin_amdgcn_s_setprio(0); } while (0)
; #define PG8_WAIT_V(n) asm volatile("s_waitcnt vmcnt(" #n ")" ::: "memory")
; #define PG8_WAIT_L(n) asm volatile("s_waitcnt lgkmcnt(" #n ")" ::: "memory")
; #define PG8_BAR __builtin_amdgcn_s_barrier()
; #define PG8_SCHED __builtin_amdgcn_sched_barrier(0)
; template <class Epi, class Sched, bool ALIGN_EPI = false, bool SP2 = false>
; __device__ __forceinline__ void gemm_phase(PG8_LAS unsigned char* lds, const Gemm g, const Sched& S, const Epi& E) {
;     ...
;             PG8_LDA(At, 1, 1); PG8_STAGE(PG8_SB(1, 0), b3, voffB); PG8_STAGE(PG8_SB(1, 1), b3 + hstep, voffB); PG8_STAGE(PG8_SA(1, 0), a3, voffA);
;             PG8_WAIT_V(8); PG8_WAIT_L(0); PG8_BAR; if (cur.half == 0) { PG8_MMA(1, 0, At, B0); PG8_MMA(1, 1, At, B1); } PG8_BAR; PG8_SCHED;
	s_add_i32 s10, s61, s27
	v_lshl_add_u64 v[228:229], v[228:229], 0, s[42:43]
	s_mov_b32 m0, s10
	ds_read_b128 v[182:185], v206 offset:49152
	ds_read_b128 v[186:189], v206 offset:50176
	ds_read_b128 v[190:193], v206 offset:51200
	ds_read_b128 v[194:197], v206 offset:52224
	ds_read_b128 v[198:201], v206 offset:53248
	ds_read_b128 v[208:211], v206 offset:54272
	ds_read_b128 v[212:215], v206 offset:55296
	ds_read_b128 v[216:219], v206 offset:56320
	global_load_lds_dwordx4 v[228:229], off
	s_add_i32 m0, s10, 0x2000
	s_add_u32 s0, s0, 0x40080
	v_lshl_add_u64 v[228:229], v[230:231], 0, s[42:43]
	s_addc_u32 s1, s1, 0
	s_add_i32 s10, s63, s27
	global_load_lds_dwordx4 v[228:229], off
	v_lshl_add_u64 v[228:229], s[0:1], 0, v[166:167]
	s_mov_b32 m0, s10
	s_nop 0
	global_load_lds_dwordx4 v[228:229], off
	v_lshl_add_u64 v[228:229], s[0:1], 0, v[170:171]
	s_add_i32 m0, s10, 0x2000
	s_nop 0
	global_load_lds_dwordx4 v[228:229], off
	v_lshl_add_u64 v[228:229], v[232:233], 0, s[42:43]
	s_mov_b32 m0, s41
	s_nop 0
	global_load_lds_dwordx4 v[228:229], off
	v_lshl_add_u64 v[228:229], v[234:235], 0, s[42:43]
	s_mov_b32 m0, s71
	s_nop 0
	global_load_lds_dwordx4 v[228:229], off
	s_waitcnt vmcnt(8)
	s_waitcnt lgkmcnt(0)
	s_barrier
	v_mfma_f32_16x16x32_bf16 v[64:67], v[132:135], v[182:185], v[64:67]
	v_mfma_f32_16x16x32_bf16 v[60:63], v[140:143], v[182:185], v[60:63]
	v_mfma_f32_16x16x32_bf16 v[48:51], v[132:135], v[190:193], v[48:51]
	v_mfma_f32_16x16x32_bf16 v[44:47], v[140:143], v[190:193], v[44:47]
	v_mfma_f32_16x16x32_bf16 v[32:35], v[132:135], v[198:201], v[32:35]
	v_mfma_f32_16x16x32_bf16 v[28:31], v[140:143], v[198:201], v[28:31]
	v_mfma_f32_16x16x32_bf16 v[16:19], v[132:135], v[212:215], v[16:19]
	v_mfma_f32_16x16x32_bf16 v[12:15], v[140:143], v[212:215], v[12:15]
	v_mfma_f32_16x16x32_bf16 v[64:67], v[136:139], v[186:189], v[64:67]
	v_mfma_f32_16x16x32_bf16 v[60:63], v[144:147], v[186:189], v[60:63]
	v_mfma_f32_16x16x32_bf16 v[48:51], v[136:139], v[194:197], v[48:51]
	v_mfma_f32_16x16x32_bf16 v[44:47], v[144:147], v[194:197], v[44:47]
	v_mfma_f32_16x16x32_bf16 v[32:35], v[136:139], v[208:211], v[32:35]
	v_mfma_f32_16x16x32_bf16 v[28:31], v[144:147], v[208:211], v[28:31]
	v_mfma_f32_16x16x32_bf16 v[16:19], v[136:139], v[216:219], v[16:19]
	v_mfma_f32_16x16x32_bf16 v[12:15], v[144:147], v[216:219], v[12:15]
	v_mfma_f32_16x16x32_bf16 v[56:59], v[148:151], v[182:185], v[56:59]
	v_mfma_f32_16x16x32_bf16 v[52:55], v[156:159], v[182:185], v[52:55]
	v_mfma_f32_16x16x32_bf16 v[40:43], v[148:151], v[190:193], v[40:43]
	v_mfma_f32_16x16x32_bf16 v[36:39], v[156:159], v[190:193], v[36:39]
	v_mfma_f32_16x16x32_bf16 v[24:27], v[148:151], v[198:201], v[24:27]
	v_mfma_f32_16x16x32_bf16 v[20:23], v[156:159], v[198:201], v[20:23]
	v_mfma_f32_16x16x32_bf16 v[8:11], v[148:151], v[212:215], v[8:11]
	v_mfma_f32_16x16x32_bf16 v[4:7], v[156:159], v[212:215], v[4:7]
	v_mfma_f32_16x16x32_bf16 v[56:59], v[152:155], v[186:189], v[56:59]
	v_mfma_f32_16x16x32_bf16 v[52:55], v[160:163], v[186:189], v[52:55]
	v_mfma_f32_16x16x32_bf16 v[40:43], v[152:155], v[194:197], v[40:43]
	v_mfma_f32_16x16x32_bf16 v[36:39], v[160:163], v[194:197], v[36:39]
	v_mfma_f32_16x16x32_bf16 v[24:27], v[152:155], v[208:211], v[24:27]
	v_mfma_f32_16x16x32_bf16 v[20:23], v[160:163], v[208:211], v[20:23]
	v_mfma_f32_16x16x32_bf16 v[8:11], v[152:155], v[216:219], v[8:11]
	v_mfma_f32_16x16x32_bf16 v[4:7], v[160:163], v[216:219], v[4:7]
	s_barrier
	s_add_i32 s39, s39, 2
	s_add_u32 s8, s8, 0x100
	s_addc_u32 s9, s9, 0
	s_add_u32 s36, s36, 0x100
	s_addc_u32 s38, s38, 0
	s_cmp_gt_u32 s39, 13
	s_cbranch_scc0 .LBB0_395
	s_and_b64 vcc, exec, s[58:59]
	s_cbranch_vccz .LBB0_398
	s_barrier

; #define PG8_STAGE(bufoff, gbase, voff) do { _Pragma("unroll") for (int _i = 0; _i < 2; ++_i) \
;         __builtin_amdgcn_global_load_lds((const unsigned*)((const char*)(gbase) + (voff)[_i]), (PG8_LAS unsigned*)(lds + (bufoff) + ldsw + _i * 8192), 16, 0, 0); } while (0)
; #define PG8_LDA(dst, b, h) do { _Pragma("unroll") for (int m = 0; m < 4; ++m) _Pragma("unroll") for (int k = 0; k < 2; ++k) dst[m][k] = *(const PG8_LAS bf16x8*)(lds + PG8_SA(b, h) + aoff + m * 2048 + k * 1024); } while (0)
; #define PG8_LDB(dst, b, h) do { _Pragma("unroll") for (int n = 0; n < 2; ++n) _Pragma("unroll") for (int k = 0; k < 2; ++k) dst[n][k] = *(const PG8_LAS bf16x8*)(lds + PG8_SB(b, h) + boff + n * 2048 + k * 1024); } while (0)
; #define PG8_MMA(ai, bj, At, Bt) do { __builtin_amdgcn_s_setprio(1); _Pragma("unroll") for (int m = 0; m < 4; ++m) _Pragma("unroll") for (int n = 0; n < 2; ++n) _Pragma("unroll") for (int k = 0; k < 2; ++k) \
;         acc[ai][bj][m][n] = __builtin_amdgcn_mfma_f32_16x16x32_bf16(Bt[n][k], At[m][k], acc[ai][bj][m][n], 0, 0, 0); __builtin_amdgcn_s_setprio(0); } while (0)
; #define PG8_WAIT_V(n) asm volatile("s_waitcnt vmcnt(" #n ")" ::: "memory")
; #define PG8_WAIT_L(n) asm volatile("s_waitcnt lgkmcnt(" #n ")" ::: "memory")
; #define PG8_BAR __builtin_amdgcn_s_barrier()
; #define PG8_SCHED __builtin_amdgcn_sched_barrier(0)
; template <class Epi, class Sched, bool ALIGN_EPI = false, bool SP2 = false>
; __device__ __forceinline__ void gemm_phase(PG8_LAS unsigned char* lds, const Gemm g, const Sched& S, const Epi& E) {
;     ...
;             PG8_LDB(B0, 0, 0); PG8_LDB(B1, 0, 1); PG8_SCHED; PG8_LDA(At, 0, 0); PG8_STAGE(PG8_SA(1, 1), a1 + hstep, voffA);
;     ...
;             if (PROBE_KIND == 18 && t == 0 && ui > 0 && g.probe) { const unsigned long long tq_ = __builtin_amdgcn_s_memrealtime(); PG8_WAIT_V(8); pg8_probe_acc += (unsigned)(__builtin_amdgcn_s_memrealtime() - tq_); }
;     ...
;             PG8_WAIT_V(8); PG8_WAIT_L(0); PG8_BAR; PG8_MMA(0, 0, At, B0); PG8_MMA(0, 1, At, B1); PG8_BAR; PG8_SCHED;
;             PG8_LDA(At, 0, 1); PG8_STAGE(PG8_SB(0, 0), b2, voffB); PG8_STAGE(PG8_SB(0, 1), b2 + hstep, voffB); PG8_STAGE(PG8_SA(0, 0), a2, voffA);
;             PG8_WAIT_V(8); PG8_WAIT_L(0); PG8_BAR; if (cur.half == 0) { PG8_MMA(1, 0, At, B0); PG8_MMA(1, 1, At, B1); } PG8_BAR; PG8_SCHED;
.LBB0_1135:
	s_add_u32 s14, s6, 0xfffe0080
	s_addc_u32 s15, s7, -1
	s_add_i32 s65, 0, 0x10000
	s_cmp_eq_u32 s64, 4
	s_cselect_b32 s21, s1, s15
	s_cselect_b32 s20, s5, s14
	s_cselect_b32 s15, s19, s63
	s_cselect_b32 s14, s39, s62
	s_add_i32 s68, 0, 0x14000
	v_add_u32_e32 v72, s65, v201
	v_add_u32_e32 v136, s68, v201
	ds_read_b128 v[36:39], v72
	ds_read_b128 v[40:43], v72 offset:1024
	ds_read_b128 v[68:71], v72 offset:2048
	ds_read_b128 v[72:75], v72 offset:3072
	ds_read_b128 v[100:103], v136
	ds_read_b128 v[104:107], v136 offset:1024
	ds_read_b128 v[132:135], v136 offset:2048
	ds_read_b128 v[136:139], v136 offset:3072
	v_lshl_add_u64 v[198:199], s[6:7], 0, v[170:171]
	s_add_i32 m0, s28, 0xc000
	ds_read_b128 v[174:177], v203
	ds_read_b128 v[178:181], v203 offset:1024
	ds_read_b128 v[182:185], v203 offset:2048
	ds_read_b128 v[186:189], v203 offset:3072
	ds_read_b128 v[190:193], v203 offset:4096
	ds_read_b128 v[194:197], v203 offset:5120
	ds_read_b128 v[204:207], v203 offset:6144
	ds_read_b128 v[208:211], v203 offset:7168
	global_load_lds_dwordx4 v[198:199], off
	v_lshl_add_u64 v[198:199], s[6:7], 0, v[172:173]
	s_add_i32 m0, s28, 0xe000
	s_nop 0
	global_load_lds_dwordx4 v[198:199], off
	s_waitcnt vmcnt(8)
	s_waitcnt lgkmcnt(0)
	s_barrier
	v_mfma_f32_16x16x32_bf16 v[56:59], v[36:39], v[174:177], v[56:59]
	v_mfma_f32_16x16x32_bf16 v[52:55], v[68:71], v[174:177], v[52:55]
	v_mfma_f32_16x16x32_bf16 v[88:91], v[36:39], v[182:185], v[88:91]
	v_mfma_f32_16x16x32_bf16 v[84:87], v[68:71], v[182:185], v[84:87]
	v_mfma_f32_16x16x32_bf16 v[120:123], v[36:39], v[190:193], v[120:123]
	v_mfma_f32_16x16x32_bf16 v[116:119], v[68:71], v[190:193], v[116:119]
	v_mfma_f32_16x16x32_bf16 v[128:131], v[36:39], v[204:207], v[128:131]
	v_mfma_f32_16x16x32_bf16 v[124:127], v[68:71], v[204:207], v[124:127]
	v_mfma_f32_16x16x32_bf16 v[56:59], v[40:43], v[178:181], v[56:59]
	v_mfma_f32_16x16x32_bf16 v[52:55], v[72:75], v[178:181], v[52:55]
	v_mfma_f32_16x16x32_bf16 v[88:91], v[40:43], v[186:189], v[88:91]
	v_mfma_f32_16x16x32_bf16 v[84:87], v[72:75], v[186:189], v[84:87]
	v_mfma_f32_16x16x32_bf16 v[120:123], v[40:43], v[194:197], v[120:123]
	v_mfma_f32_16x16x32_bf16 v[116:119], v[72:75], v[194:197], v[116:119]
	v_mfma_f32_16x16x32_bf16 v[128:131], v[40:43], v[208:211], v[128:131]
	v_mfma_f32_16x16x32_bf16 v[124:127], v[72:75], v[208:211], v[124:127]
	v_mfma_f32_16x16x32_bf16 v[160:163], v[100:103], v[174:177], v[160:163]
	v_mfma_f32_16x16x32_bf16 v[156:159], v[132:135], v[174:177], v[156:159]
	v_mfma_f32_16x16x32_bf16 v[152:155], v[100:103], v[182:185], v[152:155]
	v_mfma_f32_16x16x32_bf16 v[148:151], v[132:135], v[182:185], v[148:151]
	v_mfma_f32_16x16x32_bf16 v[144:147], v[100:103], v[190:193], v[144:147]
	v_mfma_f32_16x16x32_bf16 v[140:143], v[132:135], v[190:193], v[140:143]
	v_mfma_f32_16x16x32_bf16 v[112:115], v[100:103], v[204:207], v[112:115]
	v_mfma_f32_16x16x32_bf16 v[108:111], v[132:135], v[204:207], v[108:111]
	v_mfma_f32_16x16x32_bf16 v[160:163], v[104:107], v[178:181], v[160:163]
	v_mfma_f32_16x16x32_bf16 v[156:159], v[136:139], v[178:181], v[156:159]
	v_mfma_f32_16x16x32_bf16 v[152:155], v[104:107], v[186:189], v[152:155]
	v_mfma_f32_16x16x32_bf16 v[148:151], v[136:139], v[186:189], v[148:151]
	v_mfma_f32_16x16x32_bf16 v[144:147], v[104:107], v[194:197], v[144:147]
	v_mfma_f32_16x16x32_bf16 v[140:143], v[136:139], v[194:197], v[140:143]
	v_mfma_f32_16x16x32_bf16 v[112:115], v[104:107], v[208:211], v[112:115]
	v_mfma_f32_16x16x32_bf16 v[108:111], v[136:139], v[208:211], v[108:111]
	s_barrier
	s_add_i32 s65, s65, s27
	v_lshl_add_u64 v[198:199], s[14:15], 0, v[2:3]
	s_mov_b32 m0, s65
	ds_read_b128 v[174:177], v203 offset:16384
	ds_read_b128 v[178:181], v203 offset:17408
	ds_read_b128 v[182:185], v203 offset:18432
	ds_read_b128 v[186:189], v203 offset:19456
	ds_read_b128 v[190:193], v203 offset:20480
	ds_read_b128 v[194:197], v203 offset:21504
	ds_read_b128 v[204:207], v203 offset:22528
	ds_read_b128 v[208:211], v203 offset:23552
	global_load_lds_dwordx4 v[198:199], off
	s_add_i32 m0, s65, 0x2000
	s_add_u32 s66, s14, 0x20000
	v_lshl_add_u64 v[212:213], s[14:15], 0, v[168:169]
	s_addc_u32 s67, s15, 0
	s_add_i32 s65, s68, s27
	global_load_lds_dwordx4 v[212:213], off
	v_lshl_add_u64 v[214:215], s[66:67], 0, v[2:3]
	s_mov_b32 m0, s65
	v_lshl_add_u64 v[216:217], s[20:21], 0, v[166:167]
	global_load_lds_dwordx4 v[214:215], off
	v_lshl_add_u64 v[214:215], s[66:67], 0, v[168:169]
	s_add_i32 m0, s65, 0x2000
	s_nop 0
	global_load_lds_dwordx4 v[214:215], off
	v_lshl_add_u64 v[214:215], s[20:21], 0, v[164:165]
	s_mov_b32 m0, s28
	s_nop 0
	global_load_lds_dwordx4 v[214:215], off
	s_mov_b32 m0, s29
	s_nop 0
	global_load_lds_dwordx4 v[216:217], off
	s_waitcnt vmcnt(8)
	s_waitcnt lgkmcnt(0)
	s_barrier
; #define PG8_STAGE(bufoff, gbase, voff) do { _Pragma("unroll") for (int _i = 0; _i < 2; ++_i) \
;         __builtin_amdgcn_global_load_lds((const unsigned*)((const char*)(gbase) + (voff)[_i]), (PG8_LAS unsigned*)(lds + (bufoff) + ldsw + _i * 8192), 16, 0, 0); } while (0)
; #define PG8_LDA(dst, b, h) do { _Pragma("unroll") for (int m = 0; m < 4; ++m) _Pragma("unroll") for (int k = 0; k < 2; ++k) dst[m][k] = *(const PG8_LAS bf16x8*)(lds + PG8_SA(b, h) + aoff + m * 2048 + k * 1024); } while (0)
; #define PG8_LDB(dst, b, h) do { _Pragma("unroll") for (int n = 0; n < 2; ++n) _Pragma("unroll") for (int k = 0; k < 2; ++k) dst[n][k] = *(const PG8_LAS bf16x8*)(lds + PG8_SB(b, h) + boff + n * 2048 + k * 1024); } while (0)
; #define PG8_MMA(ai, bj, At, Bt) do { __builtin_amdgcn_s_setprio(1); _Pragma("unroll") for (int m = 0; m < 4; ++m) _Pragma("unroll") for (int n = 0; n < 2; ++n) _Pragma("unroll") for (int k = 0; k < 2; ++k) \
;         acc[ai][bj][m][n] = __builtin_amdgcn_mfma_f32_16x16x32_bf16(Bt[n][k], At[m][k], acc[ai][bj][m][n], 0, 0, 0); __builtin_amdgcn_s_setprio(0); } while (0)
; #define PG8_WAIT_V(n) asm volatile("s_waitcnt vmcnt(" #n ")" ::: "memory")
; #define PG8_WAIT_L(n) asm volatile("s_waitcnt lgkmcnt(" #n ")" ::: "memory")
; #define PG8_BAR __builtin_amdgcn_s_barrier()
; #define PG8_SCHED __builtin_amdgcn_sched_barrier(0)
; template <class Epi, class Sched, bool ALIGN_EPI = false, bool SP2 = false>
; __device__ __forceinline__ void gemm_phase(PG8_LAS unsigned char* lds, const Gemm g, const Sched& S, const Epi& E) {
;     ...
;             PG8_WAIT_V(8); PG8_WAIT_L(0); PG8_BAR; if (cur.half == 0) { PG8_MMA(1, 0, At, B0); PG8_MMA(1, 1, At, B1); } PG8_BAR; PG8_SCHED;
;             PG8_LDB(B0, 1, 0); PG8_LDB(B1, 1, 1); PG8_SCHED; PG8_LDA(At, 1, 0); PG8_STAGE(PG8_SA(0, 1), a2 + hstep, voffA);
;             PG8_WAIT_V(8); PG8_WAIT_L(0); PG8_BAR; PG8_MMA(0, 0, At, B0); PG8_MMA(0, 1, At, B1); PG8_BAR; PG8_SCHED;
	v_mfma_f32_16x16x32_bf16 v[96:99], v[36:39], v[174:177], v[96:99]
	v_mfma_f32_16x16x32_bf16 v[92:95], v[68:71], v[174:177], v[92:95]
	v_mfma_f32_16x16x32_bf16 v[64:67], v[36:39], v[182:185], v[64:67]
	v_mfma_f32_16x16x32_bf16 v[60:63], v[68:71], v[182:185], v[60:63]
	v_mfma_f32_16x16x32_bf16 v[32:35], v[36:39], v[190:193], v[32:35]
	v_mfma_f32_16x16x32_bf16 v[28:31], v[68:71], v[190:193], v[28:31]
	v_mfma_f32_16x16x32_bf16 v[16:19], v[36:39], v[204:207], v[16:19]
	v_mfma_f32_16x16x32_bf16 v[12:15], v[68:71], v[204:207], v[12:15]
	v_mfma_f32_16x16x32_bf16 v[96:99], v[40:43], v[178:181], v[96:99]
	v_mfma_f32_16x16x32_bf16 v[92:95], v[72:75], v[178:181], v[92:95]
	v_mfma_f32_16x16x32_bf16 v[64:67], v[40:43], v[186:189], v[64:67]
	v_mfma_f32_16x16x32_bf16 v[60:63], v[72:75], v[186:189], v[60:63]
	v_mfma_f32_16x16x32_bf16 v[32:35], v[40:43], v[194:197], v[32:35]
	v_mfma_f32_16x16x32_bf16 v[28:31], v[72:75], v[194:197], v[28:31]
	v_mfma_f32_16x16x32_bf16 v[16:19], v[40:43], v[208:211], v[16:19]
	v_mfma_f32_16x16x32_bf16 v[12:15], v[72:75], v[208:211], v[12:15]
	v_mfma_f32_16x16x32_bf16 v[48:51], v[100:103], v[182:185], v[48:51]
	v_mfma_f32_16x16x32_bf16 v[44:47], v[132:135], v[182:185], v[44:47]
	v_mfma_f32_16x16x32_bf16 v[24:27], v[100:103], v[190:193], v[24:27]
	v_mfma_f32_16x16x32_bf16 v[20:23], v[132:135], v[190:193], v[20:23]
	v_mfma_f32_16x16x32_bf16 v[8:11], v[100:103], v[204:207], v[8:11]
	v_mfma_f32_16x16x32_bf16 v[4:7], v[132:135], v[204:207], v[4:7]
	v_mfma_f32_16x16x32_bf16 v[36:39], v[100:103], v[174:177], v[80:83]
	v_mfma_f32_16x16x32_bf16 v[40:43], v[132:135], v[174:177], v[76:79]
	v_mfma_f32_16x16x32_bf16 v[48:51], v[104:107], v[186:189], v[48:51]
	v_mfma_f32_16x16x32_bf16 v[44:47], v[136:139], v[186:189], v[44:47]
	v_mfma_f32_16x16x32_bf16 v[24:27], v[104:107], v[194:197], v[24:27]
	v_mfma_f32_16x16x32_bf16 v[20:23], v[136:139], v[194:197], v[20:23]
	v_mfma_f32_16x16x32_bf16 v[8:11], v[104:107], v[208:211], v[8:11]
	v_mfma_f32_16x16x32_bf16 v[4:7], v[136:139], v[208:211], v[4:7]
	v_mfma_f32_16x16x32_bf16 v[36:39], v[104:107], v[178:181], v[36:39]
	v_mfma_f32_16x16x32_bf16 v[40:43], v[136:139], v[178:181], v[40:43]
	s_barrier
	s_add_i32 s65, 0, 0x18000
	s_add_i32 s66, 0, 0x1c000
	v_add_u32_e32 v80, s65, v201
	v_add_u32_e32 v136, s66, v201
	ds_read_b128 v[68:71], v80
	ds_read_b128 v[72:75], v80 offset:1024
	ds_read_b128 v[76:79], v80 offset:2048
	ds_read_b128 v[80:83], v80 offset:3072
	ds_read_b128 v[100:103], v136
	ds_read_b128 v[104:107], v136 offset:1024
	ds_read_b128 v[132:135], v136 offset:2048
	ds_read_b128 v[136:139], v136 offset:3072
	s_add_u32 s20, s20, 0x20000
	s_addc_u32 s21, s21, 0
	s_mov_b32 m0, s30
	v_lshl_add_u64 v[218:219], s[20:21], 0, v[164:165]
	ds_read_b128 v[174:177], v203 offset:32768
	ds_read_b128 v[178:181], v203 offset:33792
	ds_read_b128 v[182:185], v203 offset:34816
	ds_read_b128 v[186:189], v203 offset:35840
	ds_read_b128 v[190:193], v203 offset:36864
	ds_read_b128 v[194:197], v203 offset:37888
	ds_read_b128 v[204:207], v203 offset:38912
	ds_read_b128 v[208:211], v203 offset:39936
	global_load_lds_dwordx4 v[218:219], off
	v_lshl_add_u64 v[218:219], s[20:21], 0, v[166:167]
	s_mov_b32 m0, s31
	s_nop 0
	global_load_lds_dwordx4 v[218:219], off
	s_waitcnt vmcnt(8)
	s_waitcnt lgkmcnt(0)
	s_barrier
; #define MG_LOAD(c, buf) do { _Pragma("unroll") for (int m2 = 0; m2 < 2; ++m2) _Pragma("unroll") for (int bj = 0; bj < 2; ++bj) { \
;             const size_t ro = (size_t)(row0 + ((c) >> 1) * HALF + (2 * ((c) & 1) + m2) * 16) * DM + col0 + bj * HALF; ga[buf][m2][bj] = *(const u32x2*)(GAx + (ro & amask)); gb[buf][m2][bj] = *(const u32x2*)(GB + ro); } } while (0)
; #define PG8_STAGE(bufoff, gbase, voff) do { _Pragma("unroll") for (int _i = 0; _i < 2; ++_i) \
;         __builtin_amdgcn_global_load_lds((const unsigned*)((const char*)(gbase) + (voff)[_i]), (PG8_LAS unsigned*)(lds + (bufoff) + ldsw + _i * 8192), 16, 0, 0); } while (0)
; #define PG8_LDA(dst, b, h) do { _Pragma("unroll") for (int m = 0; m < 4; ++m) _Pragma("unroll") for (int k = 0; k < 2; ++k) dst[m][k] = *(const PG8_LAS bf16x8*)(lds + PG8_SA(b, h) + aoff + m * 2048 + k * 1024); } while (0)
; #define PG8_MMA(ai, bj, At, Bt) do { __builtin_amdgcn_s_setprio(1); _Pragma("unroll") for (int m = 0; m < 4; ++m) _Pragma("unroll") for (int n = 0; n < 2; ++n) _Pragma("unroll") for (int k = 0; k < 2; ++k) \
;         acc[ai][bj][m][n] = __builtin_amdgcn_mfma_f32_16x16x32_bf16(Bt[n][k], At[m][k], acc[ai][bj][m][n], 0, 0, 0); __builtin_amdgcn_s_setprio(0); } while (0)
; #define PG8_WAIT_V(n) asm volatile("s_waitcnt vmcnt(" #n ")" ::: "memory")
; #define PG8_WAIT_L(n) asm volatile("s_waitcnt lgkmcnt(" #n ")" ::: "memory")
; #define PG8_BAR __builtin_amdgcn_s_barrier()
; #define PG8_SCHED __builtin_amdgcn_sched_barrier(0)
;     __device__ __forceinline__ void operator()(f32x4 (&acc)[2][2][4][2], const Unit& u, int wr, int wc, int fr, int fq) const {
;     ...
;         MG_LOAD(0, 0); MG_LOAD(1, 1);
; template <class Epi, class Sched, bool ALIGN_EPI = false, bool SP2 = false>
; __device__ __forceinline__ void gemm_phase(PG8_LAS unsigned char* lds, const Gemm g, const Sched& S, const Epi& E) {
;     ...
;             PG8_WAIT_V(8); PG8_WAIT_L(0); PG8_BAR; PG8_MMA(0, 0, At, B0); PG8_MMA(0, 1, At, B1); PG8_BAR; PG8_SCHED;
;             PG8_LDA(At, 1, 1); PG8_STAGE(PG8_SB(1, 0), b3, voffB); PG8_STAGE(PG8_SB(1, 1), b3 + hstep, voffB); PG8_STAGE(PG8_SA(1, 0), a3, voffA);
;             PG8_WAIT_V(8); PG8_WAIT_L(0); PG8_BAR; if (cur.half == 0) { PG8_MMA(1, 0, At, B0); PG8_MMA(1, 1, At, B1); } PG8_BAR; PG8_SCHED;
	v_mfma_f32_16x16x32_bf16 v[56:59], v[68:71], v[174:177], v[56:59]
	v_mfma_f32_16x16x32_bf16 v[52:55], v[76:79], v[174:177], v[52:55]
	v_mfma_f32_16x16x32_bf16 v[88:91], v[68:71], v[182:185], v[88:91]
	v_mfma_f32_16x16x32_bf16 v[84:87], v[76:79], v[182:185], v[84:87]
	v_mfma_f32_16x16x32_bf16 v[120:123], v[68:71], v[190:193], v[120:123]
	v_mfma_f32_16x16x32_bf16 v[116:119], v[76:79], v[190:193], v[116:119]
	v_mfma_f32_16x16x32_bf16 v[128:131], v[68:71], v[204:207], v[128:131]
	v_mfma_f32_16x16x32_bf16 v[124:127], v[76:79], v[204:207], v[124:127]
	v_mfma_f32_16x16x32_bf16 v[56:59], v[72:75], v[178:181], v[56:59]
	v_mfma_f32_16x16x32_bf16 v[52:55], v[80:83], v[178:181], v[52:55]
	v_mfma_f32_16x16x32_bf16 v[88:91], v[72:75], v[186:189], v[88:91]
	v_mfma_f32_16x16x32_bf16 v[84:87], v[80:83], v[186:189], v[84:87]
	v_mfma_f32_16x16x32_bf16 v[120:123], v[72:75], v[194:197], v[120:123]
	v_mfma_f32_16x16x32_bf16 v[116:119], v[80:83], v[194:197], v[116:119]
	v_mfma_f32_16x16x32_bf16 v[128:131], v[72:75], v[208:211], v[128:131]
	v_mfma_f32_16x16x32_bf16 v[124:127], v[80:83], v[208:211], v[124:127]
	v_mfma_f32_16x16x32_bf16 v[160:163], v[100:103], v[174:177], v[160:163]
	v_mfma_f32_16x16x32_bf16 v[156:159], v[132:135], v[174:177], v[156:159]
	v_mfma_f32_16x16x32_bf16 v[152:155], v[100:103], v[182:185], v[152:155]
	v_mfma_f32_16x16x32_bf16 v[148:151], v[132:135], v[182:185], v[148:151]
	v_mfma_f32_16x16x32_bf16 v[144:147], v[100:103], v[190:193], v[144:147]
	v_mfma_f32_16x16x32_bf16 v[140:143], v[132:135], v[190:193], v[140:143]
	v_mfma_f32_16x16x32_bf16 v[112:115], v[100:103], v[204:207], v[112:115]
	v_mfma_f32_16x16x32_bf16 v[108:111], v[132:135], v[204:207], v[108:111]
	v_mfma_f32_16x16x32_bf16 v[160:163], v[104:107], v[178:181], v[160:163]
	v_mfma_f32_16x16x32_bf16 v[156:159], v[136:139], v[178:181], v[156:159]
	v_mfma_f32_16x16x32_bf16 v[152:155], v[104:107], v[186:189], v[152:155]
	v_mfma_f32_16x16x32_bf16 v[148:151], v[136:139], v[186:189], v[148:151]
	v_mfma_f32_16x16x32_bf16 v[144:147], v[104:107], v[194:197], v[144:147]
	v_mfma_f32_16x16x32_bf16 v[140:143], v[136:139], v[194:197], v[140:143]
	v_mfma_f32_16x16x32_bf16 v[112:115], v[104:107], v[208:211], v[112:115]
	v_mfma_f32_16x16x32_bf16 v[108:111], v[136:139], v[208:211], v[108:111]
	s_barrier
	s_add_i32 s20, s65, s27
	v_lshl_add_u64 v[198:199], v[198:199], 0, s[42:43]
	s_mov_b32 m0, s20
	ds_read_b128 v[174:177], v203 offset:49152
	ds_read_b128 v[178:181], v203 offset:50176
	ds_read_b128 v[182:185], v203 offset:51200
	ds_read_b128 v[186:189], v203 offset:52224
	ds_read_b128 v[190:193], v203 offset:53248
	ds_read_b128 v[194:197], v203 offset:54272
	ds_read_b128 v[204:207], v203 offset:55296
	ds_read_b128 v[208:211], v203 offset:56320
	global_load_lds_dwordx4 v[198:199], off
	s_add_i32 m0, s20, 0x2000
	s_add_u32 s14, s14, 0x20080
	v_lshl_add_u64 v[198:199], v[212:213], 0, s[42:43]
	s_addc_u32 s15, s15, 0
	s_add_i32 s20, s66, s27
	global_load_lds_dwordx4 v[198:199], off
	v_lshl_add_u64 v[198:199], s[14:15], 0, v[2:3]
	s_mov_b32 m0, s20
	s_nop 0
	global_load_lds_dwordx4 v[198:199], off
	v_lshl_add_u64 v[198:199], s[14:15], 0, v[168:169]
	s_add_i32 m0, s20, 0x2000
	s_nop 0
	global_load_lds_dwordx4 v[198:199], off
	v_lshl_add_u64 v[198:199], v[214:215], 0, s[42:43]
	s_mov_b32 m0, s36
	s_nop 0
	global_load_lds_dwordx4 v[198:199], off
	v_lshl_add_u64 v[198:199], v[216:217], 0, s[42:43]
	s_mov_b32 m0, s40
	s_nop 0
	global_load_lds_dwordx4 v[198:199], off
	s_waitcnt vmcnt(8)
	s_cmp_lg_u32 s64, 4
	s_cbranch_scc1 .Lmg_nopf
	s_lshl_b32 s20, s4, 8
	s_lshl_b32 s21, s0, 8
	s_cmp_gt_i32 s0, 3
	s_cbranch_scc1 .Lmg_pf2
	v_add_u32_e32 v253, s20, v200
	v_or_b32_e32 v252, s21, v202
	v_lshl_add_u32 v252, v253, 10, v252
	global_load_dwordx2 v[228:229], v252, s[10:11]
	global_load_dwordx2 v[232:233], v252, s[34:35]
	global_load_dwordx2 v[230:231], v252, s[10:11] offset:128
	global_load_dwordx2 v[234:235], v252, s[34:35] offset:128
	v_add_u32_e32 v252, 0x4000, v252
	global_load_dwordx2 v[236:237], v252, s[10:11]
	global_load_dwordx2 v[240:241], v252, s[34:35]
	global_load_dwordx2 v[238:239], v252, s[10:11] offset:128
	global_load_dwordx2 v[242:243], v252, s[34:35] offset:128
	v_add_u32_e32 v252, 0x4000, v252
	global_load_dwordx2 v[244:245], v252, s[10:11]
	global_load_dwordx2 v[248:249], v252, s[34:35]
	global_load_dwordx2 v[246:247], v252, s[10:11] offset:128
	global_load_dwordx2 v[250:251], v252, s[34:35] offset:128
	s_branch .Lmg_nopf

;     __device__ __forceinline__ void a_ready(const Unit&) const { if (++ncall == 3 && sig != nullptr && threadIdx.x == 0) __hip_atomic_fetch_add(sig, 1u, __ATOMIC_RELAXED, __HIP_MEMORY_SCOPE_AGENT); }
; #define PG8_LDA(dst, b, h) do { _Pragma("unroll") for (int m = 0; m < 4; ++m) _Pragma("unroll") for (int k = 0; k < 2; ++k) dst[m][k] = *(const PG8_LAS bf16x8*)(lds + PG8_SA(b, h) + aoff + m * 2048 + k * 1024); } while (0)
; template <class Epi, class Sched, bool ALIGN_EPI = false, bool SP2 = false>
; __device__ __forceinline__ void gemm_phase(PG8_LAS unsigned char* lds, const Gemm g, const Sched& S, const Epi& E) {
;     ...
;         for (int t = 0; t < nt; t += 2) {
;             const bool last = (t == nt - 2);
;             const char* a1 = cA + (size_t)(t + 1) * kstep;
;             const char* a2 = last ? nA : cA + (size_t)(t + 2) * kstep; const char* b2 = last ? nB : cB + (size_t)(t + 2) * kstep;
;             const char* a3 = a2 + kstep; const char* b3 = b2 + kstep;
;             if (last && has_next) S.a_ready(nxt);
;             if constexpr (SP2) {
;             PG8_LDB(B0, 0, 0); PG8_LDB(B1, 0, 1); PG8_SCHED; PG8_LDA(At, 0, 0); PG8_STAGE(PG8_SA(1, 1), a1 + hstep, voffA);
;     ...
;             if (PROBE_KIND == 18 && t == 0 && ui > 0 && g.probe) { const unsigned long long tq_ = __builtin_amdgcn_s_memrealtime(); PG8_WAIT_V(8); pg8_probe_acc += (unsigned)(__builtin_amdgcn_s_memrealtime() - tq_); }
;     ...
;             PG8_WAIT_V(8); PG8_WAIT_L(0); PG8_BAR; PG8_MMA(0, 0, At, B0); PG8_MMA(0, 1, At, B1); PG8_BAR; PG8_SCHED;
;             PG8_LDA(At, 0, 1); PG8_STAGE(PG8_SB(0, 0), b2, voffB); PG8_STAGE(PG8_SB(0, 1), b2 + hstep, voffB); PG8_STAGE(PG8_SA(0, 0), a2, voffA);
;             PG8_WAIT_V(8); PG8_WAIT_L(0); PG8_BAR; if (cur.half == 0) { PG8_MMA(1, 0, At, B0); PG8_MMA(1, 1, At, B1); } PG8_BAR; PG8_SCHED;
;             PG8_LDB(B0, 1, 0); PG8_LDB(B1, 1, 1); PG8_SCHED; PG8_LDA(At, 1, 0); PG8_STAGE(PG8_SA(0, 1), a2 + hstep, voffA);
;             PG8_WAIT_V(8); PG8_WAIT_L(0); PG8_BAR; PG8_MMA(0, 0, At, B0); PG8_MMA(0, 1, At, B1); PG8_BAR; PG8_SCHED;
;             PG8_LDA(At, 1, 1); PG8_STAGE(PG8_SB(1, 0), b3, voffB); PG8_STAGE(PG8_SB(1, 1), b3 + hstep, voffB); PG8_STAGE(PG8_SA(1, 0), a3, voffA);
;             PG8_WAIT_V(8); PG8_WAIT_L(0); PG8_BAR; if (cur.half == 0) { PG8_MMA(1, 0, At, B0); PG8_MMA(1, 1, At, B1); } PG8_BAR; PG8_SCHED;
.Lmg_nopf:
	s_waitcnt lgkmcnt(0)
	s_barrier
	v_mfma_f32_16x16x32_bf16 v[96:99], v[68:71], v[174:177], v[96:99]
	v_mfma_f32_16x16x32_bf16 v[92:95], v[76:79], v[174:177], v[92:95]
	v_mfma_f32_16x16x32_bf16 v[64:67], v[68:71], v[182:185], v[64:67]
	v_mfma_f32_16x16x32_bf16 v[60:63], v[76:79], v[182:185], v[60:63]
	v_mfma_f32_16x16x32_bf16 v[32:35], v[68:71], v[190:193], v[32:35]
	v_mfma_f32_16x16x32_bf16 v[28:31], v[76:79], v[190:193], v[28:31]
	v_mfma_f32_16x16x32_bf16 v[16:19], v[68:71], v[204:207], v[16:19]
	v_mfma_f32_16x16x32_bf16 v[12:15], v[76:79], v[204:207], v[12:15]
	v_mfma_f32_16x16x32_bf16 v[96:99], v[72:75], v[178:181], v[96:99]
	v_mfma_f32_16x16x32_bf16 v[92:95], v[80:83], v[178:181], v[92:95]
	v_mfma_f32_16x16x32_bf16 v[64:67], v[72:75], v[186:189], v[64:67]
	v_mfma_f32_16x16x32_bf16 v[60:63], v[80:83], v[186:189], v[60:63]
	v_mfma_f32_16x16x32_bf16 v[32:35], v[72:75], v[194:197], v[32:35]
	v_mfma_f32_16x16x32_bf16 v[28:31], v[80:83], v[194:197], v[28:31]
	v_mfma_f32_16x16x32_bf16 v[16:19], v[72:75], v[208:211], v[16:19]
	v_mfma_f32_16x16x32_bf16 v[12:15], v[80:83], v[208:211], v[12:15]
	v_mfma_f32_16x16x32_bf16 v[36:39], v[100:103], v[174:177], v[36:39]
	v_mfma_f32_16x16x32_bf16 v[80:83], v[104:107], v[178:181], v[36:39]
	v_mfma_f32_16x16x32_bf16 v[36:39], v[132:135], v[174:177], v[40:43]
	v_mfma_f32_16x16x32_bf16 v[76:79], v[136:139], v[178:181], v[36:39]
	v_mfma_f32_16x16x32_bf16 v[36:39], v[100:103], v[182:185], v[48:51]
	v_mfma_f32_16x16x32_bf16 v[48:51], v[104:107], v[186:189], v[36:39]
	v_mfma_f32_16x16x32_bf16 v[36:39], v[132:135], v[182:185], v[44:47]
	v_mfma_f32_16x16x32_bf16 v[24:27], v[100:103], v[190:193], v[24:27]
	v_mfma_f32_16x16x32_bf16 v[20:23], v[132:135], v[190:193], v[20:23]
	v_mfma_f32_16x16x32_bf16 v[8:11], v[100:103], v[204:207], v[8:11]
	v_mfma_f32_16x16x32_bf16 v[4:7], v[132:135], v[204:207], v[4:7]
	v_mfma_f32_16x16x32_bf16 v[44:47], v[136:139], v[186:189], v[36:39]
	v_mfma_f32_16x16x32_bf16 v[24:27], v[104:107], v[194:197], v[24:27]
	v_mfma_f32_16x16x32_bf16 v[20:23], v[136:139], v[194:197], v[20:23]
	v_mfma_f32_16x16x32_bf16 v[8:11], v[104:107], v[208:211], v[8:11]
	v_mfma_f32_16x16x32_bf16 v[4:7], v[136:139], v[208:211], v[4:7]
	s_barrier
	s_add_i32 s64, s64, 2
	s_add_u32 s6, s6, 0x100
	s_addc_u32 s7, s7, 0
	s_add_u32 s62, s62, 0x100
	s_addc_u32 s63, s63, 0
	s_cmp_gt_u32 s64, 5
	s_cbranch_scc0 .LBB0_1135
	s_and_b64 vcc, exec, s[16:17]
	s_cbranch_vccz .LBB0_1138
	s_barrier

;     __device__ __forceinline__ void a_ready(const Unit&) const { if (++ncall == 3 && sig != nullptr && threadIdx.x == 0) __hip_atomic_fetch_add(sig, 1u, __ATOMIC_RELAXED, __HIP_MEMORY_SCOPE_AGENT); }
; #define PG8_STAGE(bufoff, gbase, voff) do { _Pragma("unroll") for (int _i = 0; _i < 2; ++_i) \
;         __builtin_amdgcn_global_load_lds((const unsigned*)((const char*)(gbase) + (voff)[_i]), (PG8_LAS unsigned*)(lds + (bufoff) + ldsw + _i * 8192), 16, 0, 0); } while (0)
; #define PG8_LDA(dst, b, h) do { _Pragma("unroll") for (int m = 0; m < 4; ++m) _Pragma("unroll") for (int k = 0; k < 2; ++k) dst[m][k] = *(const PG8_LAS bf16x8*)(lds + PG8_SA(b, h) + aoff + m * 2048 + k * 1024); } while (0)
; #define PG8_WAIT_V(n) asm volatile("s_waitcnt vmcnt(" #n ")" ::: "memory")
; template <class Epi, class Sched, bool ALIGN_EPI = false, bool SP2 = false>
; __device__ __forceinline__ void gemm_phase(PG8_LAS unsigned char* lds, const Gemm g, const Sched& S, const Epi& E) {
;     ...
;         const char* nA = has_next ? (const char*)g.A + (size_t)nxt.pm * tstep + (nxt.half == 2 ? hstep : (size_t)0) : cA; const char* nB = has_next ? (const char*)g.Bt + (size_t)nxt.pn * tstep : cB;
;         for (int t = 0; t < nt; t += 2) {
;             const bool last = (t == nt - 2);
;             const char* a1 = cA + (size_t)(t + 1) * kstep;
;             const char* a2 = last ? nA : cA + (size_t)(t + 2) * kstep; const char* b2 = last ? nB : cB + (size_t)(t + 2) * kstep;
;             const char* a3 = a2 + kstep; const char* b3 = b2 + kstep;
;             if (last && has_next) S.a_ready(nxt);
;             if constexpr (SP2) {
;             PG8_LDB(B0, 0, 0); PG8_LDB(B1, 0, 1); PG8_SCHED; PG8_LDA(At, 0, 0); PG8_STAGE(PG8_SA(1, 1), a1 + hstep, voffA);
;     ...
;             if (PROBE_KIND == 18 && t == 0 && ui > 0 && g.probe) { const unsigned long long tq_ = __builtin_amdgcn_s_memrealtime(); PG8_WAIT_V(8); pg8_probe_acc += (unsigned)(__builtin_amdgcn_s_memrealtime() - tq_); }
;     ...
;             PG8_WAIT_V(8); PG8_WAIT_L(0); PG8_BAR; PG8_MMA(0, 0, At, B0); PG8_MMA(0, 1, At, B1); PG8_BAR; PG8_SCHED;
;             PG8_LDA(At, 0, 1); PG8_STAGE(PG8_SB(0, 0), b2, voffB); PG8_STAGE(PG8_SB(0, 1), b2 + hstep, voffB); PG8_STAGE(PG8_SA(0, 0), a2, voffA);
;             PG8_WAIT_V(8); PG8_WAIT_L(0); PG8_BAR; if (cur.half == 0) { PG8_MMA(1, 0, At, B0); PG8_MMA(1, 1, At, B1); } PG8_BAR; PG8_SCHED;
.LBB0_1300:
	s_add_u32 s28, s4, s0
	s_addc_u32 s29, s5, s1
	s_add_u32 s28, s28, 0x100
	s_addc_u32 s29, s29, 0
	s_add_u32 s67, s62, s0
	s_addc_u32 s68, s63, s1
	s_add_i32 s69, 0, 0x10000
	s_cmpk_eq_i32 s0, 0x700
	s_cselect_b32 s31, s7, s29
	s_cselect_b32 s30, s64, s28
	s_cselect_b32 s29, s11, s68
	s_cselect_b32 s28, s65, s67
	s_add_i32 s67, 0, 0x14000
	v_add_u32_e32 v162, s69, v148
	v_add_u32_e32 v178, s67, v148
	ds_read_b128 v[150:153], v162
	ds_read_b128 v[154:157], v162 offset:1024
	ds_read_b128 v[158:161], v162 offset:2048
	ds_read_b128 v[162:165], v162 offset:3072
	ds_read_b128 v[166:169], v178
	ds_read_b128 v[170:173], v178 offset:1024
	ds_read_b128 v[174:177], v178 offset:2048
	ds_read_b128 v[178:181], v178 offset:3072
	v_lshl_add_u64 v[216:217], v[142:143], 0, s[0:1]
	s_add_i32 m0, s40, 0xc000
	ds_read_b128 v[182:185], v149
	ds_read_b128 v[186:189], v149 offset:1024
	ds_read_b128 v[190:193], v149 offset:2048
	ds_read_b128 v[194:197], v149 offset:3072
	ds_read_b128 v[198:201], v149 offset:4096
	ds_read_b128 v[202:205], v149 offset:5120
	ds_read_b128 v[206:209], v149 offset:6144
	ds_read_b128 v[210:213], v149 offset:7168
	global_load_lds_dwordx4 v[216:217], off
	v_lshl_add_u64 v[216:217], v[144:145], 0, s[0:1]
	s_add_i32 m0, s40, 0xe000
	s_nop 0
	global_load_lds_dwordx4 v[216:217], off
	s_waitcnt vmcnt(8)
	s_waitcnt lgkmcnt(0)
	s_barrier
	v_mfma_f32_16x16x32_bf16 v[128:131], v[150:153], v[182:185], v[128:131]
	v_mfma_f32_16x16x32_bf16 v[124:127], v[158:161], v[182:185], v[124:127]
	v_mfma_f32_16x16x32_bf16 v[112:115], v[150:153], v[190:193], v[112:115]
	v_mfma_f32_16x16x32_bf16 v[108:111], v[158:161], v[190:193], v[108:111]
	v_mfma_f32_16x16x32_bf16 v[96:99], v[150:153], v[198:201], v[96:99]
	v_mfma_f32_16x16x32_bf16 v[92:95], v[158:161], v[198:201], v[92:95]
	v_mfma_f32_16x16x32_bf16 v[80:83], v[150:153], v[206:209], v[80:83]
	v_mfma_f32_16x16x32_bf16 v[76:79], v[158:161], v[206:209], v[76:79]
	v_mfma_f32_16x16x32_bf16 v[128:131], v[154:157], v[186:189], v[128:131]
	v_mfma_f32_16x16x32_bf16 v[124:127], v[162:165], v[186:189], v[124:127]
	v_mfma_f32_16x16x32_bf16 v[112:115], v[154:157], v[194:197], v[112:115]
	v_mfma_f32_16x16x32_bf16 v[108:111], v[162:165], v[194:197], v[108:111]
	v_mfma_f32_16x16x32_bf16 v[96:99], v[154:157], v[202:205], v[96:99]
	v_mfma_f32_16x16x32_bf16 v[92:95], v[162:165], v[202:205], v[92:95]
	v_mfma_f32_16x16x32_bf16 v[80:83], v[154:157], v[210:213], v[80:83]
	v_mfma_f32_16x16x32_bf16 v[76:79], v[162:165], v[210:213], v[76:79]
	v_mfma_f32_16x16x32_bf16 v[120:123], v[166:169], v[182:185], v[120:123]
	v_mfma_f32_16x16x32_bf16 v[116:119], v[174:177], v[182:185], v[116:119]
	v_mfma_f32_16x16x32_bf16 v[104:107], v[166:169], v[190:193], v[104:107]
	v_mfma_f32_16x16x32_bf16 v[100:103], v[174:177], v[190:193], v[100:103]
	v_mfma_f32_16x16x32_bf16 v[88:91], v[166:169], v[198:201], v[88:91]
	v_mfma_f32_16x16x32_bf16 v[84:87], v[174:177], v[198:201], v[84:87]
	v_mfma_f32_16x16x32_bf16 v[72:75], v[166:169], v[206:209], v[72:75]
	v_mfma_f32_16x16x32_bf16 v[68:71], v[174:177], v[206:209], v[68:71]
	v_mfma_f32_16x16x32_bf16 v[120:123], v[170:173], v[186:189], v[120:123]
	v_mfma_f32_16x16x32_bf16 v[116:119], v[178:181], v[186:189], v[116:119]
	v_mfma_f32_16x16x32_bf16 v[104:107], v[170:173], v[194:197], v[104:107]
	v_mfma_f32_16x16x32_bf16 v[100:103], v[178:181], v[194:197], v[100:103]
	v_mfma_f32_16x16x32_bf16 v[88:91], v[170:173], v[202:205], v[88:91]
	v_mfma_f32_16x16x32_bf16 v[84:87], v[178:181], v[202:205], v[84:87]
	v_mfma_f32_16x16x32_bf16 v[72:75], v[170:173], v[210:213], v[72:75]
	v_mfma_f32_16x16x32_bf16 v[68:71], v[178:181], v[210:213], v[68:71]
	s_barrier
	s_add_i32 s68, s69, s39
	v_lshl_add_u64 v[216:217], s[28:29], 0, v[2:3]
	s_mov_b32 m0, s68
	ds_read_b128 v[182:185], v149 offset:16384
	ds_read_b128 v[186:189], v149 offset:17408
	ds_read_b128 v[190:193], v149 offset:18432
	ds_read_b128 v[194:197], v149 offset:19456
	ds_read_b128 v[198:201], v149 offset:20480
	ds_read_b128 v[202:205], v149 offset:21504
	ds_read_b128 v[206:209], v149 offset:22528
	ds_read_b128 v[210:213], v149 offset:23552
	global_load_lds_dwordx4 v[216:217], off
	s_add_i32 m0, s68, 0x2000
	s_add_u32 s68, s28, 0x40000
	v_lshl_add_u64 v[218:219], s[28:29], 0, v[136:137]
	s_addc_u32 s69, s29, 0
	s_add_i32 s67, s67, s39
	global_load_lds_dwordx4 v[218:219], off
	v_lshl_add_u64 v[220:221], s[68:69], 0, v[2:3]
	s_mov_b32 m0, s67
	v_lshl_add_u64 v[228:229], s[30:31], 0, v[134:135]
	global_load_lds_dwordx4 v[220:221], off
	v_lshl_add_u64 v[220:221], s[68:69], 0, v[136:137]
	s_add_i32 m0, s67, 0x2000
	s_nop 0
	global_load_lds_dwordx4 v[220:221], off
	v_lshl_add_u64 v[220:221], s[30:31], 0, v[132:133]
	s_mov_b32 m0, s40
	s_nop 0
	global_load_lds_dwordx4 v[220:221], off
	s_mov_b32 m0, s41
	s_nop 0
	global_load_lds_dwordx4 v[228:229], off
	s_waitcnt vmcnt(8)
	s_waitcnt lgkmcnt(0)
	s_barrier
; #define PG8_STAGE(bufoff, gbase, voff) do { _Pragma("unroll") for (int _i = 0; _i < 2; ++_i) \
;         __builtin_amdgcn_global_load_lds((const unsigned*)((const char*)(gbase) + (voff)[_i]), (PG8_LAS unsigned*)(lds + (bufoff) + ldsw + _i * 8192), 16, 0, 0); } while (0)
; #define PG8_LDA(dst, b, h) do { _Pragma("unroll") for (int m = 0; m < 4; ++m) _Pragma("unroll") for (int k = 0; k < 2; ++k) dst[m][k] = *(const PG8_LAS bf16x8*)(lds + PG8_SA(b, h) + aoff + m * 2048 + k * 1024); } while (0)
; #define PG8_LDB(dst, b, h) do { _Pragma("unroll") for (int n = 0; n < 2; ++n) _Pragma("unroll") for (int k = 0; k < 2; ++k) dst[n][k] = *(const PG8_LAS bf16x8*)(lds + PG8_SB(b, h) + boff + n * 2048 + k * 1024); } while (0)
; #define PG8_MMA(ai, bj, At, Bt) do { __builtin_amdgcn_s_setprio(1); _Pragma("unroll") for (int m = 0; m < 4; ++m) _Pragma("unroll") for (int n = 0; n < 2; ++n) _Pragma("unroll") for (int k = 0; k < 2; ++k) \
;         acc[ai][bj][m][n] = __builtin_amdgcn_mfma_f32_16x16x32_bf16(Bt[n][k], At[m][k], acc[ai][bj][m][n], 0, 0, 0); __builtin_amdgcn_s_setprio(0); } while (0)
; #define PG8_WAIT_V(n) asm volatile("s_waitcnt vmcnt(" #n ")" ::: "memory")
; #define PG8_WAIT_L(n) asm volatile("s_waitcnt lgkmcnt(" #n ")" ::: "memory")
; #define PG8_BAR __builtin_amdgcn_s_barrier()
; #define PG8_SCHED __builtin_amdgcn_sched_barrier(0)
; template <class Epi, class Sched, bool ALIGN_EPI = false, bool SP2 = false>
; __device__ __forceinline__ void gemm_phase(PG8_LAS unsigned char* lds, const Gemm g, const Sched& S, const Epi& E) {
;     ...
;             PG8_WAIT_V(8); PG8_WAIT_L(0); PG8_BAR; if (cur.half == 0) { PG8_MMA(1, 0, At, B0); PG8_MMA(1, 1, At, B1); } PG8_BAR; PG8_SCHED;
;             PG8_LDB(B0, 1, 0); PG8_LDB(B1, 1, 1); PG8_SCHED; PG8_LDA(At, 1, 0); PG8_STAGE(PG8_SA(0, 1), a2 + hstep, voffA);
;             PG8_WAIT_V(8); PG8_WAIT_L(0); PG8_BAR; PG8_MMA(0, 0, At, B0); PG8_MMA(0, 1, At, B1); PG8_BAR; PG8_SCHED;
	v_mfma_f32_16x16x32_bf16 v[64:67], v[150:153], v[182:185], v[64:67]
	v_mfma_f32_16x16x32_bf16 v[60:63], v[158:161], v[182:185], v[60:63]
	v_mfma_f32_16x16x32_bf16 v[48:51], v[150:153], v[190:193], v[48:51]
	v_mfma_f32_16x16x32_bf16 v[44:47], v[158:161], v[190:193], v[44:47]
	v_mfma_f32_16x16x32_bf16 v[32:35], v[150:153], v[198:201], v[32:35]
	v_mfma_f32_16x16x32_bf16 v[28:31], v[158:161], v[198:201], v[28:31]
	v_mfma_f32_16x16x32_bf16 v[16:19], v[150:153], v[206:209], v[16:19]
	v_mfma_f32_16x16x32_bf16 v[12:15], v[158:161], v[206:209], v[12:15]
	v_mfma_f32_16x16x32_bf16 v[64:67], v[154:157], v[186:189], v[64:67]
	v_mfma_f32_16x16x32_bf16 v[60:63], v[162:165], v[186:189], v[60:63]
	v_mfma_f32_16x16x32_bf16 v[48:51], v[154:157], v[194:197], v[48:51]
	v_mfma_f32_16x16x32_bf16 v[44:47], v[162:165], v[194:197], v[44:47]
	v_mfma_f32_16x16x32_bf16 v[32:35], v[154:157], v[202:205], v[32:35]
	v_mfma_f32_16x16x32_bf16 v[28:31], v[162:165], v[202:205], v[28:31]
	v_mfma_f32_16x16x32_bf16 v[16:19], v[154:157], v[210:213], v[16:19]
	v_mfma_f32_16x16x32_bf16 v[12:15], v[162:165], v[210:213], v[12:15]
	v_mfma_f32_16x16x32_bf16 v[56:59], v[166:169], v[182:185], v[56:59]
	v_mfma_f32_16x16x32_bf16 v[52:55], v[174:177], v[182:185], v[52:55]
	v_mfma_f32_16x16x32_bf16 v[40:43], v[166:169], v[190:193], v[40:43]
	v_mfma_f32_16x16x32_bf16 v[36:39], v[174:177], v[190:193], v[36:39]
	v_mfma_f32_16x16x32_bf16 v[24:27], v[166:169], v[198:201], v[24:27]
	v_mfma_f32_16x16x32_bf16 v[20:23], v[174:177], v[198:201], v[20:23]
	v_mfma_f32_16x16x32_bf16 v[8:11], v[166:169], v[206:209], v[8:11]
	v_mfma_f32_16x16x32_bf16 v[4:7], v[174:177], v[206:209], v[4:7]
	v_mfma_f32_16x16x32_bf16 v[56:59], v[170:173], v[186:189], v[56:59]
	v_mfma_f32_16x16x32_bf16 v[52:55], v[178:181], v[186:189], v[52:55]
	v_mfma_f32_16x16x32_bf16 v[40:43], v[170:173], v[194:197], v[40:43]
	v_mfma_f32_16x16x32_bf16 v[36:39], v[178:181], v[194:197], v[36:39]
	v_mfma_f32_16x16x32_bf16 v[24:27], v[170:173], v[202:205], v[24:27]
	v_mfma_f32_16x16x32_bf16 v[20:23], v[178:181], v[202:205], v[20:23]
	v_mfma_f32_16x16x32_bf16 v[8:11], v[170:173], v[210:213], v[8:11]
	v_mfma_f32_16x16x32_bf16 v[4:7], v[178:181], v[210:213], v[4:7]
	s_barrier
	s_add_i32 s67, 0, 0x18000
	s_add_i32 s68, 0, 0x1c000
	v_add_u32_e32 v162, s67, v148
	v_add_u32_e32 v178, s68, v148
	ds_read_b128 v[150:153], v162
	ds_read_b128 v[154:157], v162 offset:1024
	ds_read_b128 v[158:161], v162 offset:2048
	ds_read_b128 v[162:165], v162 offset:3072
	ds_read_b128 v[166:169], v178
	ds_read_b128 v[170:173], v178 offset:1024
	ds_read_b128 v[174:177], v178 offset:2048
	ds_read_b128 v[178:181], v178 offset:3072
	s_add_u32 s30, s30, 0x40000
	s_addc_u32 s31, s31, 0
	s_mov_b32 m0, s56
	v_lshl_add_u64 v[230:231], s[30:31], 0, v[132:133]
	ds_read_b128 v[182:185], v149 offset:32768
	ds_read_b128 v[186:189], v149 offset:33792
	ds_read_b128 v[190:193], v149 offset:34816
	ds_read_b128 v[194:197], v149 offset:35840
	ds_read_b128 v[198:201], v149 offset:36864
	ds_read_b128 v[202:205], v149 offset:37888
	ds_read_b128 v[206:209], v149 offset:38912
	ds_read_b128 v[210:213], v149 offset:39936
	global_load_lds_dwordx4 v[230:231], off
	v_lshl_add_u64 v[230:231], s[30:31], 0, v[134:135]
	s_mov_b32 m0, s57
	s_nop 0
	global_load_lds_dwordx4 v[230:231], off
	s_waitcnt vmcnt(8)
	s_waitcnt lgkmcnt(0)
	s_barrier
	v_mfma_f32_16x16x32_bf16 v[128:131], v[150:153], v[182:185], v[128:131]
	v_mfma_f32_16x16x32_bf16 v[124:127], v[158:161], v[182:185], v[124:127]
	v_mfma_f32_16x16x32_bf16 v[112:115], v[150:153], v[190:193], v[112:115]
	v_mfma_f32_16x16x32_bf16 v[108:111], v[158:161], v[190:193], v[108:111]
	v_mfma_f32_16x16x32_bf16 v[96:99], v[150:153], v[198:201], v[96:99]
	v_mfma_f32_16x16x32_bf16 v[92:95], v[158:161], v[198:201], v[92:95]
	v_mfma_f32_16x16x32_bf16 v[80:83], v[150:153], v[206:209], v[80:83]
	v_mfma_f32_16x16x32_bf16 v[76:79], v[158:161], v[206:209], v[76:79]
	v_mfma_f32_16x16x32_bf16 v[128:131], v[154:157], v[186:189], v[128:131]
	v_mfma_f32_16x16x32_bf16 v[124:127], v[162:165], v[186:189], v[124:127]
	v_mfma_f32_16x16x32_bf16 v[112:115], v[154:157], v[194:197], v[112:115]
	v_mfma_f32_16x16x32_bf16 v[108:111], v[162:165], v[194:197], v[108:111]
	v_mfma_f32_16x16x32_bf16 v[96:99], v[154:157], v[202:205], v[96:99]
	v_mfma_f32_16x16x32_bf16 v[92:95], v[162:165], v[202:205], v[92:95]
	v_mfma_f32_16x16x32_bf16 v[80:83], v[154:157], v[210:213], v[80:83]
	v_mfma_f32_16x16x32_bf16 v[76:79], v[162:165], v[210:213], v[76:79]
	v_mfma_f32_16x16x32_bf16 v[120:123], v[166:169], v[182:185], v[120:123]
	v_mfma_f32_16x16x32_bf16 v[116:119], v[174:177], v[182:185], v[116:119]
	v_mfma_f32_16x16x32_bf16 v[104:107], v[166:169], v[190:193], v[104:107]
	v_mfma_f32_16x16x32_bf16 v[100:103], v[174:177], v[190:193], v[100:103]
	v_mfma_f32_16x16x32_bf16 v[88:91], v[166:169], v[198:201], v[88:91]
	v_mfma_f32_16x16x32_bf16 v[84:87], v[174:177], v[198:201], v[84:87]
	v_mfma_f32_16x16x32_bf16 v[72:75], v[166:169], v[206:209], v[72:75]
	v_mfma_f32_16x16x32_bf16 v[68:71], v[174:177], v[206:209], v[68:71]
	v_mfma_f32_16x16x32_bf16 v[120:123], v[170:173], v[186:189], v[120:123]
	v_mfma_f32_16x16x32_bf16 v[116:119], v[178:181], v[186:189], v[116:119]
	v_mfma_f32_16x16x32_bf16 v[104:107], v[170:173], v[194:197], v[104:107]
	v_mfma_f32_16x16x32_bf16 v[100:103], v[178:181], v[194:197], v[100:103]
	v_mfma_f32_16x16x32_bf16 v[88:91], v[170:173], v[202:205], v[88:91]
	v_mfma_f32_16x16x32_bf16 v[84:87], v[178:181], v[202:205], v[84:87]
	v_mfma_f32_16x16x32_bf16 v[72:75], v[170:173], v[210:213], v[72:75]
	v_mfma_f32_16x16x32_bf16 v[68:71], v[178:181], v[210:213], v[68:71]
	s_barrier
; #define PG8_STAGE(bufoff, gbase, voff) do { _Pragma("unroll") for (int _i = 0; _i < 2; ++_i) \
;         __builtin_amdgcn_global_load_lds((const unsigned*)((const char*)(gbase) + (voff)[_i]), (PG8_LAS unsigned*)(lds + (bufoff) + ldsw + _i * 8192), 16, 0, 0); } while (0)
; #define PG8_LDA(dst, b, h) do { _Pragma("unroll") for (int m = 0; m < 4; ++m) _Pragma("unroll") for (int k = 0; k < 2; ++k) dst[m][k] = *(const PG8_LAS bf16x8*)(lds + PG8_SA(b, h) + aoff + m * 2048 + k * 1024); } while (0)
; #define PG8_MMA(ai, bj, At, Bt) do { __builtin_amdgcn_s_setprio(1); _Pragma("unroll") for (int m = 0; m < 4; ++m) _Pragma("unroll") for (int n = 0; n < 2; ++n) _Pragma("unroll") for (int k = 0; k < 2; ++k) \
;         acc[ai][bj][m][n] = __builtin_amdgcn_mfma_f32_16x16x32_bf16(Bt[n][k], At[m][k], acc[ai][bj][m][n], 0, 0, 0); __builtin_amdgcn_s_setprio(0); } while (0)
; #define PG8_WAIT_V(n) asm volatile("s_waitcnt vmcnt(" #n ")" ::: "memory")
; #define PG8_WAIT_L(n) asm volatile("s_waitcnt lgkmcnt(" #n ")" ::: "memory")
; #define PG8_BAR __builtin_amdgcn_s_barrier()
; #define PG8_SCHED __builtin_amdgcn_sched_barrier(0)
; template <class Epi, class Sched, bool ALIGN_EPI = false, bool SP2 = false>
; __device__ __forceinline__ void gemm_phase(PG8_LAS unsigned char* lds, const Gemm g, const Sched& S, const Epi& E) {
;     ...
;             PG8_LDA(At, 1, 1); PG8_STAGE(PG8_SB(1, 0), b3, voffB); PG8_STAGE(PG8_SB(1, 1), b3 + hstep, voffB); PG8_STAGE(PG8_SA(1, 0), a3, voffA);
;             PG8_WAIT_V(8); PG8_WAIT_L(0); PG8_BAR; if (cur.half == 0) { PG8_MMA(1, 0, At, B0); PG8_MMA(1, 1, At, B1); } PG8_BAR; PG8_SCHED;
;     ...
;         if (!has_next) break;
;         if constexpr (!Epi::CHAIN) {
; #pragma unroll
;         for (int a = 0; a < 2; ++a)
; #pragma unroll
;             for (int b = 0; b < 2; ++b)
; #pragma unroll
;                 for (int m = 0; m < 4; ++m)
; #pragma unroll
;                     for (int n = 0; n < 2; ++n) acc[a][b][m][n] = (f32x4){0.f, 0.f, 0.f, 0.f};
;         }
;         cur = nxt; cA = nA; cB = nB; ++ui;
	s_add_i32 s30, s67, s39
	v_lshl_add_u64 v[216:217], v[216:217], 0, s[42:43]
	s_mov_b32 m0, s30
	ds_read_b128 v[182:185], v149 offset:49152
	ds_read_b128 v[186:189], v149 offset:50176
	ds_read_b128 v[190:193], v149 offset:51200
	ds_read_b128 v[194:197], v149 offset:52224
	ds_read_b128 v[198:201], v149 offset:53248
	ds_read_b128 v[202:205], v149 offset:54272
	ds_read_b128 v[206:209], v149 offset:55296
	ds_read_b128 v[210:213], v149 offset:56320
	global_load_lds_dwordx4 v[216:217], off
	s_add_i32 m0, s30, 0x2000
	s_add_u32 s28, s28, 0x40080
	v_lshl_add_u64 v[216:217], v[218:219], 0, s[42:43]
	s_addc_u32 s29, s29, 0
	s_add_i32 s30, s68, s39
	global_load_lds_dwordx4 v[216:217], off
	v_lshl_add_u64 v[216:217], s[28:29], 0, v[2:3]
	s_mov_b32 m0, s30
	s_nop 0
	global_load_lds_dwordx4 v[216:217], off
	v_lshl_add_u64 v[216:217], s[28:29], 0, v[136:137]
	s_add_i32 m0, s30, 0x2000
	s_nop 0
	global_load_lds_dwordx4 v[216:217], off
	v_lshl_add_u64 v[216:217], v[220:221], 0, s[42:43]
	s_mov_b32 m0, s58
	s_nop 0
	global_load_lds_dwordx4 v[216:217], off
	v_lshl_add_u64 v[216:217], v[228:229], 0, s[42:43]
	s_mov_b32 m0, s59
	s_nop 0
	global_load_lds_dwordx4 v[216:217], off
	s_waitcnt vmcnt(8)
	s_waitcnt lgkmcnt(0)
	s_barrier
	v_mfma_f32_16x16x32_bf16 v[64:67], v[150:153], v[182:185], v[64:67]
	v_mfma_f32_16x16x32_bf16 v[60:63], v[158:161], v[182:185], v[60:63]
	v_mfma_f32_16x16x32_bf16 v[48:51], v[150:153], v[190:193], v[48:51]
	v_mfma_f32_16x16x32_bf16 v[44:47], v[158:161], v[190:193], v[44:47]
	v_mfma_f32_16x16x32_bf16 v[32:35], v[150:153], v[198:201], v[32:35]
	v_mfma_f32_16x16x32_bf16 v[28:31], v[158:161], v[198:201], v[28:31]
	v_mfma_f32_16x16x32_bf16 v[16:19], v[150:153], v[206:209], v[16:19]
	v_mfma_f32_16x16x32_bf16 v[12:15], v[158:161], v[206:209], v[12:15]
	v_mfma_f32_16x16x32_bf16 v[64:67], v[154:157], v[186:189], v[64:67]
	v_mfma_f32_16x16x32_bf16 v[60:63], v[162:165], v[186:189], v[60:63]
	v_mfma_f32_16x16x32_bf16 v[48:51], v[154:157], v[194:197], v[48:51]
	v_mfma_f32_16x16x32_bf16 v[44:47], v[162:165], v[194:197], v[44:47]
	v_mfma_f32_16x16x32_bf16 v[32:35], v[154:157], v[202:205], v[32:35]
	v_mfma_f32_16x16x32_bf16 v[28:31], v[162:165], v[202:205], v[28:31]
	v_mfma_f32_16x16x32_bf16 v[16:19], v[154:157], v[210:213], v[16:19]
	v_mfma_f32_16x16x32_bf16 v[12:15], v[162:165], v[210:213], v[12:15]
	v_mfma_f32_16x16x32_bf16 v[56:59], v[166:169], v[182:185], v[56:59]
	v_mfma_f32_16x16x32_bf16 v[52:55], v[174:177], v[182:185], v[52:55]
	v_mfma_f32_16x16x32_bf16 v[40:43], v[166:169], v[190:193], v[40:43]
	v_mfma_f32_16x16x32_bf16 v[36:39], v[174:177], v[190:193], v[36:39]
	v_mfma_f32_16x16x32_bf16 v[24:27], v[166:169], v[198:201], v[24:27]
	v_mfma_f32_16x16x32_bf16 v[20:23], v[174:177], v[198:201], v[20:23]
	v_mfma_f32_16x16x32_bf16 v[8:11], v[166:169], v[206:209], v[8:11]
	v_mfma_f32_16x16x32_bf16 v[4:7], v[174:177], v[206:209], v[4:7]
	v_mfma_f32_16x16x32_bf16 v[56:59], v[170:173], v[186:189], v[56:59]
	v_mfma_f32_16x16x32_bf16 v[52:55], v[178:181], v[186:189], v[52:55]
	v_mfma_f32_16x16x32_bf16 v[40:43], v[170:173], v[194:197], v[40:43]
	v_mfma_f32_16x16x32_bf16 v[36:39], v[178:181], v[194:197], v[36:39]
	v_mfma_f32_16x16x32_bf16 v[24:27], v[170:173], v[202:205], v[24:27]
	v_mfma_f32_16x16x32_bf16 v[20:23], v[178:181], v[202:205], v[20:23]
	v_mfma_f32_16x16x32_bf16 v[8:11], v[170:173], v[210:213], v[8:11]
	v_mfma_f32_16x16x32_bf16 v[4:7], v[178:181], v[210:213], v[4:7]
	s_barrier
	s_add_i32 s66, s66, 2
	s_add_u32 s0, s0, 0x100
	s_addc_u32 s1, s1, 0
	s_cmp_gt_u32 s66, 13
	s_cbranch_scc0 .LBB0_1300
	s_add_u32 s0, s62, 0xffffff00
	s_addc_u32 s1, s63, -1
	s_andn2_b64 vcc, exec, s[20:21]
	s_cbranch_vccnz .LBB0_1303
	v_mov_b32_e32 v4, 0
	s_mov_b32 s16, s10
	s_mov_b32 s8, s6
	s_mov_b64 s[4:5], s[26:27]
	s_mov_b32 s60, s61
	v_mov_b32_e32 v5, v4
	v_mov_b32_e32 v6, v4
	v_mov_b32_e32 v7, v4
	v_mov_b32_e32 v8, v4
	v_mov_b32_e32 v9, v4
	v_mov_b32_e32 v10, v4
	v_mov_b32_e32 v11, v4
	v_mov_b32_e32 v20, v4
	v_mov_b32_e32 v21, v4
	v_mov_b32_e32 v22, v4
	v_mov_b32_e32 v23, v4
	v_mov_b32_e32 v24, v4
	v_mov_b32_e32 v25, v4
	v_mov_b32_e32 v26, v4
	v_mov_b32_e32 v27, v4
	v_mov_b32_e32 v36, v4
	v_mov_b32_e32 v37, v4
	v_mov_b32_e32 v38, v4
	v_mov_b32_e32 v39, v4
	v_mov_b32_e32 v40, v4
	v_mov_b32_e32 v41, v4
	v_mov_b32_e32 v42, v4
	v_mov_b32_e32 v43, v4
	v_mov_b32_e32 v52, v4
	v_mov_b32_e32 v53, v4
	v_mov_b32_e32 v54, v4
	v_mov_b32_e32 v55, v4
	v_mov_b32_e32 v56, v4
	v_mov_b32_e32 v57, v4
	v_mov_b32_e32 v58, v4
	v_mov_b32_e32 v59, v4
	v_mov_b32_e32 v12, v4
	v_mov_b32_e32 v13, v4
	v_mov_b32_e32 v14, v4
	v_mov_b32_e32 v15, v4
	v_mov_b32_e32 v16, v4
	v_mov_b32_e32 v17, v4
	v_mov_b32_e32 v18, v4
	v_mov_b32_e32 v19, v4
	v_mov_b32_e32 v28, v4
	v_mov_b32_e32 v29, v4
	v_mov_b32_e32 v30, v4
	v_mov_b32_e32 v31, v4
	v_mov_b32_e32 v32, v4
	v_mov_b32_e32 v33, v4
	v_mov_b32_e32 v34, v4
	v_mov_b32_e32 v35, v4
	v_mov_b32_e32 v44, v4
	v_mov_b32_e32 v45, v4
	v_mov_b32_e32 v46, v4
	v_mov_b32_e32 v47, v4
	v_mov_b32_e32 v48, v4
	v_mov_b32_e32 v49, v4
	v_mov_b32_e32 v50, v4
	v_mov_b32_e32 v51, v4
	v_mov_b32_e32 v60, v4
	v_mov_b32_e32 v61, v4
	v_mov_b32_e32 v62, v4
	v_mov_b32_e32 v63, v4
	v_mov_b32_e32 v64, v4
	v_mov_b32_e32 v65, v4
	v_mov_b32_e32 v66, v4
	v_mov_b32_e32 v67, v4
	v_mov_b32_e32 v68, v4
	v_mov_b32_e32 v69, v4
	v_mov_b32_e32 v70, v4
	v_mov_b32_e32 v71, v4
	v_mov_b32_e32 v72, v4
	v_mov_b32_e32 v73, v4
	v_mov_b32_e32 v74, v4
	v_mov_b32_e32 v75, v4
	v_mov_b32_e32 v84, v4
	v_mov_b32_e32 v85, v4
	v_mov_b32_e32 v86, v4
	v_mov_b32_e32 v87, v4
	v_mov_b32_e32 v88, v4
	v_mov_b32_e32 v89, v4
	v_mov_b32_e32 v90, v4
	v_mov_b32_e32 v91, v4
	v_mov_b32_e32 v100, v4
	v_mov_b32_e32 v101, v4
	v_mov_b32_e32 v102, v4
	v_mov_b32_e32 v103, v4
	v_mov_b32_e32 v104, v4
	v_mov_b32_e32 v105, v4
	v_mov_b32_e32 v106, v4
	v_mov_b32_e32 v107, v4
	v_mov_b32_e32 v116, v4
	v_mov_b32_e32 v117, v4
	v_mov_b32_e32 v118, v4
	v_mov_b32_e32 v119, v4
	v_mov_b32_e32 v120, v4
	v_mov_b32_e32 v121, v4
	v_mov_b32_e32 v122, v4
	v_mov_b32_e32 v123, v4
	v_mov_b32_e32 v76, v4
	v_mov_b32_e32 v77, v4
	v_mov_b32_e32 v78, v4
	v_mov_b32_e32 v79, v4
	v_mov_b32_e32 v80, v4
	v_mov_b32_e32 v81, v4
	v_mov_b32_e32 v82, v4
	v_mov_b32_e32 v83, v4
	v_mov_b32_e32 v92, v4
	v_mov_b32_e32 v93, v4
	v_mov_b32_e32 v94, v4
	v_mov_b32_e32 v95, v4
	v_mov_b32_e32 v96, v4
	v_mov_b32_e32 v97, v4
	v_mov_b32_e32 v98, v4
	v_mov_b32_e32 v99, v4
	v_mov_b32_e32 v108, v4
	v_mov_b32_e32 v109, v4
	v_mov_b32_e32 v110, v4
	v_mov_b32_e32 v111, v4
	v_mov_b32_e32 v112, v4
	v_mov_b32_e32 v113, v4
	v_mov_b32_e32 v114, v4
	v_mov_b32_e32 v115, v4
	v_mov_b32_e32 v124, v4
	v_mov_b32_e32 v125, v4
	v_mov_b32_e32 v126, v4
	v_mov_b32_e32 v127, v4
	v_mov_b32_e32 v128, v4
	v_mov_b32_e32 v129, v4
	v_mov_b32_e32 v130, v4
	v_mov_b32_e32 v131, v4
	s_andn2_b64 vcc, exec, s[14:15]
	s_cbranch_vccnz .LBB0_1304
	s_branch .LBB0_1305

;     __device__ __forceinline__ void a_ready(const Unit&) const { if (++ncall == 3 && sig != nullptr && threadIdx.x == 0) __hip_atomic_fetch_add(sig, 1u, __ATOMIC_RELAXED, __HIP_MEMORY_SCOPE_AGENT); }
; #define PG8_STAGE(bufoff, gbase, voff) do { _Pragma("unroll") for (int _i = 0; _i < 2; ++_i) \
;         __builtin_amdgcn_global_load_lds((const unsigned*)((const char*)(gbase) + (voff)[_i]), (PG8_LAS unsigned*)(lds + (bufoff) + ldsw + _i * 8192), 16, 0, 0); } while (0)
; #define PG8_LDA(dst, b, h) do { _Pragma("unroll") for (int m = 0; m < 4; ++m) _Pragma("unroll") for (int k = 0; k < 2; ++k) dst[m][k] = *(const PG8_LAS bf16x8*)(lds + PG8_SA(b, h) + aoff + m * 2048 + k * 1024); } while (0)
; #define PG8_WAIT_V(n) asm volatile("s_waitcnt vmcnt(" #n ")" ::: "memory")
; template <class Epi, class Sched, bool ALIGN_EPI = false, bool SP2 = false>
; __device__ __forceinline__ void gemm_phase(PG8_LAS unsigned char* lds, const Gemm g, const Sched& S, const Epi& E) {
;     ...
;         const char* nA = has_next ? (const char*)g.A + (size_t)nxt.pm * tstep + (nxt.half == 2 ? hstep : (size_t)0) : cA; const char* nB = has_next ? (const char*)g.Bt + (size_t)nxt.pn * tstep : cB;
;         for (int t = 0; t < nt; t += 2) {
;             const bool last = (t == nt - 2);
;             const char* a1 = cA + (size_t)(t + 1) * kstep;
;             const char* a2 = last ? nA : cA + (size_t)(t + 2) * kstep; const char* b2 = last ? nB : cB + (size_t)(t + 2) * kstep;
;             const char* a3 = a2 + kstep; const char* b3 = b2 + kstep;
;             if (last && has_next) S.a_ready(nxt);
;             if constexpr (SP2) {
;             PG8_LDB(B0, 0, 0); PG8_LDB(B1, 0, 1); PG8_SCHED; PG8_LDA(At, 0, 0); PG8_STAGE(PG8_SA(1, 1), a1 + hstep, voffA);
;     ...
;             if (PROBE_KIND == 18 && t == 0 && ui > 0 && g.probe) { const unsigned long long tq_ = __builtin_amdgcn_s_memrealtime(); PG8_WAIT_V(8); pg8_probe_acc += (unsigned)(__builtin_amdgcn_s_memrealtime() - tq_); }
;     ...
;             PG8_WAIT_V(8); PG8_WAIT_L(0); PG8_BAR; PG8_MMA(0, 0, At, B0); PG8_MMA(0, 1, At, B1); PG8_BAR; PG8_SCHED;
;             PG8_LDA(At, 0, 1); PG8_STAGE(PG8_SB(0, 0), b2, voffB); PG8_STAGE(PG8_SB(0, 1), b2 + hstep, voffB); PG8_STAGE(PG8_SA(0, 0), a2, voffA);
;             PG8_WAIT_V(8); PG8_WAIT_L(0); PG8_BAR; if (cur.half == 0) { PG8_MMA(1, 0, At, B0); PG8_MMA(1, 1, At, B1); } PG8_BAR; PG8_SCHED;
.LBB0_1477:
	s_add_u32 s0, s26, 0xfffc0080
	s_addc_u32 s1, s27, -1
	s_add_i32 s67, 0, 0x10000
	s_cmp_eq_u32 s66, 12
	s_cselect_b32 s29, s17, s1
	s_cselect_b32 s28, s62, s0
	v_add_u32_e32 v151, s67, v147
	s_cselect_b32 s1, s19, s65
	s_cselect_b32 s0, s63, s64
	s_add_i32 s70, 0, 0x14000
	ds_read_b128 v[142:145], v151
	ds_read_b128 v[152:155], v151 offset:1024
	ds_read_b128 v[156:159], v151 offset:2048
	ds_read_b128 v[160:163], v151 offset:3072
	v_add_u32_e32 v151, s70, v147
	ds_read_b128 v[164:167], v151
	ds_read_b128 v[168:171], v151 offset:1024
	ds_read_b128 v[172:175], v151 offset:2048
	ds_read_b128 v[176:179], v151 offset:3072
	v_lshl_add_u64 v[212:213], s[26:27], 0, v[138:139]
	s_add_i32 m0, s15, 0xc000
	ds_read_b128 v[180:183], v150
	ds_read_b128 v[184:187], v150 offset:1024
	ds_read_b128 v[188:191], v150 offset:2048
	ds_read_b128 v[192:195], v150 offset:3072
	ds_read_b128 v[196:199], v150 offset:4096
	ds_read_b128 v[200:203], v150 offset:5120
	ds_read_b128 v[204:207], v150 offset:6144
	ds_read_b128 v[208:211], v150 offset:7168
	global_load_lds_dwordx4 v[212:213], off
	v_lshl_add_u64 v[212:213], s[26:27], 0, v[140:141]
	s_add_i32 m0, s15, 0xe000
	s_nop 0
	global_load_lds_dwordx4 v[212:213], off
	s_waitcnt vmcnt(8)
	s_waitcnt lgkmcnt(0)
	s_barrier
	v_mfma_f32_16x16x32_bf16 v[128:131], v[142:145], v[180:183], v[128:131]
	v_mfma_f32_16x16x32_bf16 v[124:127], v[156:159], v[180:183], v[124:127]
	v_mfma_f32_16x16x32_bf16 v[112:115], v[142:145], v[188:191], v[112:115]
	v_mfma_f32_16x16x32_bf16 v[108:111], v[156:159], v[188:191], v[108:111]
	v_mfma_f32_16x16x32_bf16 v[96:99], v[142:145], v[196:199], v[96:99]
	v_mfma_f32_16x16x32_bf16 v[92:95], v[156:159], v[196:199], v[92:95]
	v_mfma_f32_16x16x32_bf16 v[80:83], v[142:145], v[204:207], v[80:83]
	v_mfma_f32_16x16x32_bf16 v[76:79], v[156:159], v[204:207], v[76:79]
	v_mfma_f32_16x16x32_bf16 v[128:131], v[152:155], v[184:187], v[128:131]
	v_mfma_f32_16x16x32_bf16 v[124:127], v[160:163], v[184:187], v[124:127]
	v_mfma_f32_16x16x32_bf16 v[112:115], v[152:155], v[192:195], v[112:115]
	v_mfma_f32_16x16x32_bf16 v[108:111], v[160:163], v[192:195], v[108:111]
	v_mfma_f32_16x16x32_bf16 v[96:99], v[152:155], v[200:203], v[96:99]
	v_mfma_f32_16x16x32_bf16 v[92:95], v[160:163], v[200:203], v[92:95]
	v_mfma_f32_16x16x32_bf16 v[80:83], v[152:155], v[208:211], v[80:83]
	v_mfma_f32_16x16x32_bf16 v[76:79], v[160:163], v[208:211], v[76:79]
	v_mfma_f32_16x16x32_bf16 v[120:123], v[164:167], v[180:183], v[120:123]
	v_mfma_f32_16x16x32_bf16 v[116:119], v[172:175], v[180:183], v[116:119]
	v_mfma_f32_16x16x32_bf16 v[104:107], v[164:167], v[188:191], v[104:107]
	v_mfma_f32_16x16x32_bf16 v[100:103], v[172:175], v[188:191], v[100:103]
	v_mfma_f32_16x16x32_bf16 v[88:91], v[164:167], v[196:199], v[88:91]
	v_mfma_f32_16x16x32_bf16 v[84:87], v[172:175], v[196:199], v[84:87]
	v_mfma_f32_16x16x32_bf16 v[72:75], v[164:167], v[204:207], v[72:75]
	v_mfma_f32_16x16x32_bf16 v[68:71], v[172:175], v[204:207], v[68:71]
	v_mfma_f32_16x16x32_bf16 v[120:123], v[168:171], v[184:187], v[120:123]
	v_mfma_f32_16x16x32_bf16 v[116:119], v[176:179], v[184:187], v[116:119]
	v_mfma_f32_16x16x32_bf16 v[104:107], v[168:171], v[192:195], v[104:107]
	v_mfma_f32_16x16x32_bf16 v[100:103], v[176:179], v[192:195], v[100:103]
	v_mfma_f32_16x16x32_bf16 v[88:91], v[168:171], v[200:203], v[88:91]
	v_mfma_f32_16x16x32_bf16 v[84:87], v[176:179], v[200:203], v[84:87]
	v_mfma_f32_16x16x32_bf16 v[72:75], v[168:171], v[208:211], v[72:75]
	v_mfma_f32_16x16x32_bf16 v[68:71], v[176:179], v[208:211], v[68:71]
	s_barrier
	s_add_i32 s67, s67, s25
	v_lshl_add_u64 v[212:213], s[0:1], 0, v[2:3]
	s_mov_b32 m0, s67
	ds_read_b128 v[180:183], v150 offset:16384
	ds_read_b128 v[184:187], v150 offset:17408
	ds_read_b128 v[188:191], v150 offset:18432
	ds_read_b128 v[192:195], v150 offset:19456
	ds_read_b128 v[196:199], v150 offset:20480
	ds_read_b128 v[200:203], v150 offset:21504
	ds_read_b128 v[204:207], v150 offset:22528
	ds_read_b128 v[208:211], v150 offset:23552
	global_load_lds_dwordx4 v[212:213], off
	s_add_i32 m0, s67, 0x2000
	s_add_u32 s68, s0, 0x40000
	v_lshl_add_u64 v[214:215], s[0:1], 0, v[136:137]
	s_addc_u32 s69, s1, 0
	s_add_i32 s67, s70, s25
	global_load_lds_dwordx4 v[214:215], off
	v_lshl_add_u64 v[216:217], s[68:69], 0, v[2:3]
	s_mov_b32 m0, s67
	v_lshl_add_u64 v[218:219], s[28:29], 0, v[134:135]
	global_load_lds_dwordx4 v[216:217], off
	v_lshl_add_u64 v[216:217], s[68:69], 0, v[136:137]
	s_add_i32 m0, s67, 0x2000
	s_nop 0
	global_load_lds_dwordx4 v[216:217], off
	v_lshl_add_u64 v[216:217], s[28:29], 0, v[132:133]
	s_mov_b32 m0, s15
	s_nop 0
	global_load_lds_dwordx4 v[216:217], off
	s_mov_b32 m0, s21
	s_nop 0
	global_load_lds_dwordx4 v[218:219], off
	s_waitcnt vmcnt(8)
	s_waitcnt lgkmcnt(0)
	s_barrier
; #define PG8_STAGE(bufoff, gbase, voff) do { _Pragma("unroll") for (int _i = 0; _i < 2; ++_i) \
;         __builtin_amdgcn_global_load_lds((const unsigned*)((const char*)(gbase) + (voff)[_i]), (PG8_LAS unsigned*)(lds + (bufoff) + ldsw + _i * 8192), 16, 0, 0); } while (0)
; #define PG8_LDA(dst, b, h) do { _Pragma("unroll") for (int m = 0; m < 4; ++m) _Pragma("unroll") for (int k = 0; k < 2; ++k) dst[m][k] = *(const PG8_LAS bf16x8*)(lds + PG8_SA(b, h) + aoff + m * 2048 + k * 1024); } while (0)
; #define PG8_LDB(dst, b, h) do { _Pragma("unroll") for (int n = 0; n < 2; ++n) _Pragma("unroll") for (int k = 0; k < 2; ++k) dst[n][k] = *(const PG8_LAS bf16x8*)(lds + PG8_SB(b, h) + boff + n * 2048 + k * 1024); } while (0)
; #define PG8_MMA(ai, bj, At, Bt) do { __builtin_amdgcn_s_setprio(1); _Pragma("unroll") for (int m = 0; m < 4; ++m) _Pragma("unroll") for (int n = 0; n < 2; ++n) _Pragma("unroll") for (int k = 0; k < 2; ++k) \
;         acc[ai][bj][m][n] = __builtin_amdgcn_mfma_f32_16x16x32_bf16(Bt[n][k], At[m][k], acc[ai][bj][m][n], 0, 0, 0); __builtin_amdgcn_s_setprio(0); } while (0)
; #define PG8_WAIT_V(n) asm volatile("s_waitcnt vmcnt(" #n ")" ::: "memory")
; #define PG8_WAIT_L(n) asm volatile("s_waitcnt lgkmcnt(" #n ")" ::: "memory")
; #define PG8_BAR __builtin_amdgcn_s_barrier()
; #define PG8_SCHED __builtin_amdgcn_sched_barrier(0)
; template <class Epi, class Sched, bool ALIGN_EPI = false, bool SP2 = false>
; __device__ __forceinline__ void gemm_phase(PG8_LAS unsigned char* lds, const Gemm g, const Sched& S, const Epi& E) {
;     ...
;             PG8_WAIT_V(8); PG8_WAIT_L(0); PG8_BAR; if (cur.half == 0) { PG8_MMA(1, 0, At, B0); PG8_MMA(1, 1, At, B1); } PG8_BAR; PG8_SCHED;
;             PG8_LDB(B0, 1, 0); PG8_LDB(B1, 1, 1); PG8_SCHED; PG8_LDA(At, 1, 0); PG8_STAGE(PG8_SA(0, 1), a2 + hstep, voffA);
;             PG8_WAIT_V(8); PG8_WAIT_L(0); PG8_BAR; PG8_MMA(0, 0, At, B0); PG8_MMA(0, 1, At, B1); PG8_BAR; PG8_SCHED;
	v_mfma_f32_16x16x32_bf16 v[64:67], v[142:145], v[180:183], v[64:67]
	v_mfma_f32_16x16x32_bf16 v[60:63], v[156:159], v[180:183], v[60:63]
	v_mfma_f32_16x16x32_bf16 v[48:51], v[142:145], v[188:191], v[48:51]
	v_mfma_f32_16x16x32_bf16 v[44:47], v[156:159], v[188:191], v[44:47]
	v_mfma_f32_16x16x32_bf16 v[32:35], v[142:145], v[196:199], v[32:35]
	v_mfma_f32_16x16x32_bf16 v[28:31], v[156:159], v[196:199], v[28:31]
	v_mfma_f32_16x16x32_bf16 v[16:19], v[142:145], v[204:207], v[16:19]
	v_mfma_f32_16x16x32_bf16 v[12:15], v[156:159], v[204:207], v[12:15]
	v_mfma_f32_16x16x32_bf16 v[64:67], v[152:155], v[184:187], v[64:67]
	v_mfma_f32_16x16x32_bf16 v[60:63], v[160:163], v[184:187], v[60:63]
	v_mfma_f32_16x16x32_bf16 v[48:51], v[152:155], v[192:195], v[48:51]
	v_mfma_f32_16x16x32_bf16 v[44:47], v[160:163], v[192:195], v[44:47]
	v_mfma_f32_16x16x32_bf16 v[32:35], v[152:155], v[200:203], v[32:35]
	v_mfma_f32_16x16x32_bf16 v[28:31], v[160:163], v[200:203], v[28:31]
	v_mfma_f32_16x16x32_bf16 v[16:19], v[152:155], v[208:211], v[16:19]
	v_mfma_f32_16x16x32_bf16 v[12:15], v[160:163], v[208:211], v[12:15]
	v_mfma_f32_16x16x32_bf16 v[56:59], v[164:167], v[180:183], v[56:59]
	v_mfma_f32_16x16x32_bf16 v[52:55], v[172:175], v[180:183], v[52:55]
	v_mfma_f32_16x16x32_bf16 v[40:43], v[164:167], v[188:191], v[40:43]
	v_mfma_f32_16x16x32_bf16 v[36:39], v[172:175], v[188:191], v[36:39]
	v_mfma_f32_16x16x32_bf16 v[24:27], v[164:167], v[196:199], v[24:27]
	v_mfma_f32_16x16x32_bf16 v[20:23], v[172:175], v[196:199], v[20:23]
	v_mfma_f32_16x16x32_bf16 v[8:11], v[164:167], v[204:207], v[8:11]
	v_mfma_f32_16x16x32_bf16 v[4:7], v[172:175], v[204:207], v[4:7]
	v_mfma_f32_16x16x32_bf16 v[56:59], v[168:171], v[184:187], v[56:59]
	v_mfma_f32_16x16x32_bf16 v[52:55], v[176:179], v[184:187], v[52:55]
	v_mfma_f32_16x16x32_bf16 v[40:43], v[168:171], v[192:195], v[40:43]
	v_mfma_f32_16x16x32_bf16 v[36:39], v[176:179], v[192:195], v[36:39]
	v_mfma_f32_16x16x32_bf16 v[24:27], v[168:171], v[200:203], v[24:27]
	v_mfma_f32_16x16x32_bf16 v[20:23], v[176:179], v[200:203], v[20:23]
	v_mfma_f32_16x16x32_bf16 v[8:11], v[168:171], v[208:211], v[8:11]
	v_mfma_f32_16x16x32_bf16 v[4:7], v[176:179], v[208:211], v[4:7]
	s_barrier
	s_add_i32 s67, 0, 0x18000
	v_add_u32_e32 v151, s67, v147
	s_add_i32 s68, 0, 0x1c000
	ds_read_b128 v[142:145], v151
	ds_read_b128 v[152:155], v151 offset:1024
	ds_read_b128 v[156:159], v151 offset:2048
	ds_read_b128 v[160:163], v151 offset:3072
	v_add_u32_e32 v151, s68, v147
	ds_read_b128 v[164:167], v151
	ds_read_b128 v[168:171], v151 offset:1024
	ds_read_b128 v[172:175], v151 offset:2048
	ds_read_b128 v[176:179], v151 offset:3072
	s_add_u32 s28, s28, 0x40000
	s_addc_u32 s29, s29, 0
	s_mov_b32 m0, s36
	v_lshl_add_u64 v[220:221], s[28:29], 0, v[132:133]
	ds_read_b128 v[180:183], v150 offset:32768
	ds_read_b128 v[184:187], v150 offset:33792
	ds_read_b128 v[188:191], v150 offset:34816
	ds_read_b128 v[192:195], v150 offset:35840
	ds_read_b128 v[196:199], v150 offset:36864
	ds_read_b128 v[200:203], v150 offset:37888
	ds_read_b128 v[204:207], v150 offset:38912
	ds_read_b128 v[208:211], v150 offset:39936
	global_load_lds_dwordx4 v[220:221], off
	v_lshl_add_u64 v[220:221], s[28:29], 0, v[134:135]
	s_mov_b32 m0, s40
	s_nop 0
	global_load_lds_dwordx4 v[220:221], off
	s_waitcnt vmcnt(8)
	s_waitcnt lgkmcnt(0)
	s_barrier
	v_mfma_f32_16x16x32_bf16 v[128:131], v[142:145], v[180:183], v[128:131]
	v_mfma_f32_16x16x32_bf16 v[124:127], v[156:159], v[180:183], v[124:127]
	v_mfma_f32_16x16x32_bf16 v[112:115], v[142:145], v[188:191], v[112:115]
	v_mfma_f32_16x16x32_bf16 v[108:111], v[156:159], v[188:191], v[108:111]
	v_mfma_f32_16x16x32_bf16 v[96:99], v[142:145], v[196:199], v[96:99]
	v_mfma_f32_16x16x32_bf16 v[92:95], v[156:159], v[196:199], v[92:95]
	v_mfma_f32_16x16x32_bf16 v[80:83], v[142:145], v[204:207], v[80:83]
	v_mfma_f32_16x16x32_bf16 v[76:79], v[156:159], v[204:207], v[76:79]
	v_mfma_f32_16x16x32_bf16 v[128:131], v[152:155], v[184:187], v[128:131]
	v_mfma_f32_16x16x32_bf16 v[124:127], v[160:163], v[184:187], v[124:127]
	v_mfma_f32_16x16x32_bf16 v[112:115], v[152:155], v[192:195], v[112:115]
	v_mfma_f32_16x16x32_bf16 v[108:111], v[160:163], v[192:195], v[108:111]
	v_mfma_f32_16x16x32_bf16 v[96:99], v[152:155], v[200:203], v[96:99]
	v_mfma_f32_16x16x32_bf16 v[92:95], v[160:163], v[200:203], v[92:95]
	v_mfma_f32_16x16x32_bf16 v[80:83], v[152:155], v[208:211], v[80:83]
	v_mfma_f32_16x16x32_bf16 v[76:79], v[160:163], v[208:211], v[76:79]
	v_mfma_f32_16x16x32_bf16 v[120:123], v[164:167], v[180:183], v[120:123]
	v_mfma_f32_16x16x32_bf16 v[116:119], v[172:175], v[180:183], v[116:119]
	v_mfma_f32_16x16x32_bf16 v[104:107], v[164:167], v[188:191], v[104:107]
	v_mfma_f32_16x16x32_bf16 v[100:103], v[172:175], v[188:191], v[100:103]
	v_mfma_f32_16x16x32_bf16 v[88:91], v[164:167], v[196:199], v[88:91]
	v_mfma_f32_16x16x32_bf16 v[84:87], v[172:175], v[196:199], v[84:87]
	v_mfma_f32_16x16x32_bf16 v[72:75], v[164:167], v[204:207], v[72:75]
	v_mfma_f32_16x16x32_bf16 v[68:71], v[172:175], v[204:207], v[68:71]
	v_mfma_f32_16x16x32_bf16 v[120:123], v[168:171], v[184:187], v[120:123]
	v_mfma_f32_16x16x32_bf16 v[116:119], v[176:179], v[184:187], v[116:119]
	v_mfma_f32_16x16x32_bf16 v[104:107], v[168:171], v[192:195], v[104:107]
	v_mfma_f32_16x16x32_bf16 v[100:103], v[176:179], v[192:195], v[100:103]
	v_mfma_f32_16x16x32_bf16 v[88:91], v[168:171], v[200:203], v[88:91]
	v_mfma_f32_16x16x32_bf16 v[84:87], v[176:179], v[200:203], v[84:87]
	v_mfma_f32_16x16x32_bf16 v[72:75], v[168:171], v[208:211], v[72:75]
	v_mfma_f32_16x16x32_bf16 v[68:71], v[176:179], v[208:211], v[68:71]
	s_barrier
; #define PG8_STAGE(bufoff, gbase, voff) do { _Pragma("unroll") for (int _i = 0; _i < 2; ++_i) \
;         __builtin_amdgcn_global_load_lds((const unsigned*)((const char*)(gbase) + (voff)[_i]), (PG8_LAS unsigned*)(lds + (bufoff) + ldsw + _i * 8192), 16, 0, 0); } while (0)
; #define PG8_LDA(dst, b, h) do { _Pragma("unroll") for (int m = 0; m < 4; ++m) _Pragma("unroll") for (int k = 0; k < 2; ++k) dst[m][k] = *(const PG8_LAS bf16x8*)(lds + PG8_SA(b, h) + aoff + m * 2048 + k * 1024); } while (0)
; #define PG8_MMA(ai, bj, At, Bt) do { __builtin_amdgcn_s_setprio(1); _Pragma("unroll") for (int m = 0; m < 4; ++m) _Pragma("unroll") for (int n = 0; n < 2; ++n) _Pragma("unroll") for (int k = 0; k < 2; ++k) \
;         acc[ai][bj][m][n] = __builtin_amdgcn_mfma_f32_16x16x32_bf16(Bt[n][k], At[m][k], acc[ai][bj][m][n], 0, 0, 0); __builtin_amdgcn_s_setprio(0); } while (0)
; #define PG8_WAIT_V(n) asm volatile("s_waitcnt vmcnt(" #n ")" ::: "memory")
; #define PG8_WAIT_L(n) asm volatile("s_waitcnt lgkmcnt(" #n ")" ::: "memory")
; #define PG8_BAR __builtin_amdgcn_s_barrier()
; #define PG8_SCHED __builtin_amdgcn_sched_barrier(0)
; template <class Epi, class Sched, bool ALIGN_EPI = false, bool SP2 = false>
; __device__ __forceinline__ void gemm_phase(PG8_LAS unsigned char* lds, const Gemm g, const Sched& S, const Epi& E) {
;     ...
;             PG8_LDA(At, 1, 1); PG8_STAGE(PG8_SB(1, 0), b3, voffB); PG8_STAGE(PG8_SB(1, 1), b3 + hstep, voffB); PG8_STAGE(PG8_SA(1, 0), a3, voffA);
;             PG8_WAIT_V(8); PG8_WAIT_L(0); PG8_BAR; if (cur.half == 0) { PG8_MMA(1, 0, At, B0); PG8_MMA(1, 1, At, B1); } PG8_BAR; PG8_SCHED;
	s_add_i32 s28, s67, s25
	v_lshl_add_u64 v[212:213], v[212:213], 0, s[42:43]
	s_mov_b32 m0, s28
	ds_read_b128 v[180:183], v150 offset:49152
	ds_read_b128 v[184:187], v150 offset:50176
	ds_read_b128 v[188:191], v150 offset:51200
	ds_read_b128 v[192:195], v150 offset:52224
	ds_read_b128 v[196:199], v150 offset:53248
	ds_read_b128 v[200:203], v150 offset:54272
	ds_read_b128 v[204:207], v150 offset:55296
	ds_read_b128 v[208:211], v150 offset:56320
	global_load_lds_dwordx4 v[212:213], off
	s_add_i32 m0, s28, 0x2000
	s_add_u32 s0, s0, 0x40080
	v_lshl_add_u64 v[212:213], v[214:215], 0, s[42:43]
	s_addc_u32 s1, s1, 0
	s_add_i32 s28, s68, s25
	global_load_lds_dwordx4 v[212:213], off
	v_lshl_add_u64 v[212:213], s[0:1], 0, v[2:3]
	s_mov_b32 m0, s28
	s_nop 0
	global_load_lds_dwordx4 v[212:213], off
	v_lshl_add_u64 v[212:213], s[0:1], 0, v[136:137]
	s_add_i32 m0, s28, 0x2000
	s_nop 0
	global_load_lds_dwordx4 v[212:213], off
	v_lshl_add_u64 v[212:213], v[216:217], 0, s[42:43]
	s_mov_b32 m0, s41
	s_nop 0
	global_load_lds_dwordx4 v[212:213], off
	v_lshl_add_u64 v[212:213], v[218:219], 0, s[42:43]
	s_mov_b32 m0, s60
	s_nop 0
	global_load_lds_dwordx4 v[212:213], off
	s_waitcnt vmcnt(8)
	s_waitcnt lgkmcnt(0)
	s_barrier
	v_mfma_f32_16x16x32_bf16 v[64:67], v[142:145], v[180:183], v[64:67]
	v_mfma_f32_16x16x32_bf16 v[60:63], v[156:159], v[180:183], v[60:63]
	v_mfma_f32_16x16x32_bf16 v[48:51], v[142:145], v[188:191], v[48:51]
	v_mfma_f32_16x16x32_bf16 v[44:47], v[156:159], v[188:191], v[44:47]
	v_mfma_f32_16x16x32_bf16 v[32:35], v[142:145], v[196:199], v[32:35]
	v_mfma_f32_16x16x32_bf16 v[28:31], v[156:159], v[196:199], v[28:31]
	v_mfma_f32_16x16x32_bf16 v[16:19], v[142:145], v[204:207], v[16:19]
	v_mfma_f32_16x16x32_bf16 v[12:15], v[156:159], v[204:207], v[12:15]
	v_mfma_f32_16x16x32_bf16 v[64:67], v[152:155], v[184:187], v[64:67]
	v_mfma_f32_16x16x32_bf16 v[60:63], v[160:163], v[184:187], v[60:63]
	v_mfma_f32_16x16x32_bf16 v[48:51], v[152:155], v[192:195], v[48:51]
	v_mfma_f32_16x16x32_bf16 v[44:47], v[160:163], v[192:195], v[44:47]
	v_mfma_f32_16x16x32_bf16 v[32:35], v[152:155], v[200:203], v[32:35]
	v_mfma_f32_16x16x32_bf16 v[28:31], v[160:163], v[200:203], v[28:31]
	v_mfma_f32_16x16x32_bf16 v[16:19], v[152:155], v[208:211], v[16:19]
	v_mfma_f32_16x16x32_bf16 v[12:15], v[160:163], v[208:211], v[12:15]
	v_mfma_f32_16x16x32_bf16 v[56:59], v[164:167], v[180:183], v[56:59]
	v_mfma_f32_16x16x32_bf16 v[52:55], v[172:175], v[180:183], v[52:55]
	v_mfma_f32_16x16x32_bf16 v[40:43], v[164:167], v[188:191], v[40:43]
	v_mfma_f32_16x16x32_bf16 v[36:39], v[172:175], v[188:191], v[36:39]
	v_mfma_f32_16x16x32_bf16 v[24:27], v[164:167], v[196:199], v[24:27]
	v_mfma_f32_16x16x32_bf16 v[20:23], v[172:175], v[196:199], v[20:23]
	v_mfma_f32_16x16x32_bf16 v[8:11], v[164:167], v[204:207], v[8:11]
	v_mfma_f32_16x16x32_bf16 v[4:7], v[172:175], v[204:207], v[4:7]
	v_mfma_f32_16x16x32_bf16 v[56:59], v[168:171], v[184:187], v[56:59]
	v_mfma_f32_16x16x32_bf16 v[52:55], v[176:179], v[184:187], v[52:55]
	v_mfma_f32_16x16x32_bf16 v[40:43], v[168:171], v[192:195], v[40:43]
	v_mfma_f32_16x16x32_bf16 v[36:39], v[176:179], v[192:195], v[36:39]
	v_mfma_f32_16x16x32_bf16 v[24:27], v[168:171], v[200:203], v[24:27]
	v_mfma_f32_16x16x32_bf16 v[20:23], v[176:179], v[200:203], v[20:23]
	v_mfma_f32_16x16x32_bf16 v[8:11], v[168:171], v[208:211], v[8:11]
	v_mfma_f32_16x16x32_bf16 v[4:7], v[176:179], v[208:211], v[4:7]
	s_barrier
	s_add_i32 s66, s66, 2
	s_add_u32 s26, s26, 0x100
	s_addc_u32 s27, s27, 0
	s_add_u32 s64, s64, 0x100
	s_addc_u32 s65, s65, 0
	s_cmp_gt_u32 s66, 13
	s_cbranch_scc0 .LBB0_1477
	s_and_b64 vcc, exec, s[12:13]
	s_cbranch_vccz .LBB0_1480
	s_barrier

;     __device__ __forceinline__ void a_ready(const Unit&) const { if (++ncall == 3 && sig != nullptr && threadIdx.x == 0) __hip_atomic_fetch_add(sig, 1u, __ATOMIC_RELAXED, __HIP_MEMORY_SCOPE_AGENT); }
; #define PG8_STAGE(bufoff, gbase, voff) do { _Pragma("unroll") for (int _i = 0; _i < 2; ++_i) \
;         __builtin_amdgcn_global_load_lds((const unsigned*)((const char*)(gbase) + (voff)[_i]), (PG8_LAS unsigned*)(lds + (bufoff) + ldsw + _i * 8192), 16, 0, 0); } while (0)
; #define PG8_LDA(dst, b, h) do { _Pragma("unroll") for (int m = 0; m < 4; ++m) _Pragma("unroll") for (int k = 0; k < 2; ++k) dst[m][k] = *(const PG8_LAS bf16x8*)(lds + PG8_SA(b, h) + aoff + m * 2048 + k * 1024); } while (0)
; #define PG8_WAIT_V(n) asm volatile("s_waitcnt vmcnt(" #n ")" ::: "memory")
; template <class Epi, class Sched, bool ALIGN_EPI = false, bool SP2 = false>
; __device__ __forceinline__ void gemm_phase(PG8_LAS unsigned char* lds, const Gemm g, const Sched& S, const Epi& E) {
;     ...
;         const char* nA = has_next ? (const char*)g.A + (size_t)nxt.pm * tstep + (nxt.half == 2 ? hstep : (size_t)0) : cA; const char* nB = has_next ? (const char*)g.Bt + (size_t)nxt.pn * tstep : cB;
;         for (int t = 0; t < nt; t += 2) {
;             const bool last = (t == nt - 2);
;             const char* a1 = cA + (size_t)(t + 1) * kstep;
;             const char* a2 = last ? nA : cA + (size_t)(t + 2) * kstep; const char* b2 = last ? nB : cB + (size_t)(t + 2) * kstep;
;             const char* a3 = a2 + kstep; const char* b3 = b2 + kstep;
;             if (last && has_next) S.a_ready(nxt);
;             if constexpr (SP2) {
;             PG8_LDB(B0, 0, 0); PG8_LDB(B1, 0, 1); PG8_SCHED; PG8_LDA(At, 0, 0); PG8_STAGE(PG8_SA(1, 1), a1 + hstep, voffA);
;     ...
;             if (PROBE_KIND == 18 && t == 0 && ui > 0 && g.probe) { const unsigned long long tq_ = __builtin_amdgcn_s_memrealtime(); PG8_WAIT_V(8); pg8_probe_acc += (unsigned)(__builtin_amdgcn_s_memrealtime() - tq_); }
;     ...
;             PG8_WAIT_V(8); PG8_WAIT_L(0); PG8_BAR; PG8_MMA(0, 0, At, B0); PG8_MMA(0, 1, At, B1); PG8_BAR; PG8_SCHED;
;             PG8_LDA(At, 0, 1); PG8_STAGE(PG8_SB(0, 0), b2, voffB); PG8_STAGE(PG8_SB(0, 1), b2 + hstep, voffB); PG8_STAGE(PG8_SA(0, 0), a2, voffA);
;             PG8_WAIT_V(8); PG8_WAIT_L(0); PG8_BAR; if (cur.half == 0) { PG8_MMA(1, 0, At, B0); PG8_MMA(1, 1, At, B1); } PG8_BAR; PG8_SCHED;
.LBB0_1780:
	s_add_u32 s18, s6, s0
	s_addc_u32 s19, s7, s1
	s_add_u32 s18, s18, 0x100
	s_addc_u32 s19, s19, 0
	s_add_u32 s63, s60, s0
	s_addc_u32 s64, s61, s1
	s_add_i32 s65, 0, 0x10000
	s_cmpk_eq_i32 s0, 0x1500
	s_cselect_b32 s21, s15, s19
	s_cselect_b32 s20, s14, s18
	s_cselect_b32 s19, s11, s64
	s_cselect_b32 s18, s10, s63
	s_add_i32 s63, 0, 0x14000
	v_add_u32_e32 v162, s65, v148
	v_add_u32_e32 v178, s63, v148
	ds_read_b128 v[150:153], v162
	ds_read_b128 v[154:157], v162 offset:1024
	ds_read_b128 v[158:161], v162 offset:2048
	ds_read_b128 v[162:165], v162 offset:3072
	ds_read_b128 v[166:169], v178
	ds_read_b128 v[170:173], v178 offset:1024
	ds_read_b128 v[174:177], v178 offset:2048
	ds_read_b128 v[178:181], v178 offset:3072
	v_lshl_add_u64 v[214:215], v[142:143], 0, s[0:1]
	s_add_i32 m0, s35, 0xc000
	ds_read_b128 v[182:185], v149
	ds_read_b128 v[186:189], v149 offset:1024
	ds_read_b128 v[190:193], v149 offset:2048
	ds_read_b128 v[194:197], v149 offset:3072
	ds_read_b128 v[198:201], v149 offset:4096
	ds_read_b128 v[202:205], v149 offset:5120
	ds_read_b128 v[206:209], v149 offset:6144
	ds_read_b128 v[210:213], v149 offset:7168
	global_load_lds_dwordx4 v[214:215], off
	v_lshl_add_u64 v[214:215], v[144:145], 0, s[0:1]
	s_add_i32 m0, s35, 0xe000
	s_nop 0
	global_load_lds_dwordx4 v[214:215], off
	s_waitcnt vmcnt(8)
	s_waitcnt lgkmcnt(0)
	s_barrier
	v_mfma_f32_16x16x32_bf16 v[128:131], v[150:153], v[182:185], v[128:131]
	v_mfma_f32_16x16x32_bf16 v[124:127], v[158:161], v[182:185], v[124:127]
	v_mfma_f32_16x16x32_bf16 v[112:115], v[150:153], v[190:193], v[112:115]
	v_mfma_f32_16x16x32_bf16 v[108:111], v[158:161], v[190:193], v[108:111]
	v_mfma_f32_16x16x32_bf16 v[96:99], v[150:153], v[198:201], v[96:99]
	v_mfma_f32_16x16x32_bf16 v[92:95], v[158:161], v[198:201], v[92:95]
	v_mfma_f32_16x16x32_bf16 v[80:83], v[150:153], v[206:209], v[80:83]
	v_mfma_f32_16x16x32_bf16 v[76:79], v[158:161], v[206:209], v[76:79]
	v_mfma_f32_16x16x32_bf16 v[128:131], v[154:157], v[186:189], v[128:131]
	v_mfma_f32_16x16x32_bf16 v[124:127], v[162:165], v[186:189], v[124:127]
	v_mfma_f32_16x16x32_bf16 v[112:115], v[154:157], v[194:197], v[112:115]
	v_mfma_f32_16x16x32_bf16 v[108:111], v[162:165], v[194:197], v[108:111]
	v_mfma_f32_16x16x32_bf16 v[96:99], v[154:157], v[202:205], v[96:99]
	v_mfma_f32_16x16x32_bf16 v[92:95], v[162:165], v[202:205], v[92:95]
	v_mfma_f32_16x16x32_bf16 v[80:83], v[154:157], v[210:213], v[80:83]
	v_mfma_f32_16x16x32_bf16 v[76:79], v[162:165], v[210:213], v[76:79]
	v_mfma_f32_16x16x32_bf16 v[120:123], v[166:169], v[182:185], v[120:123]
	v_mfma_f32_16x16x32_bf16 v[116:119], v[174:177], v[182:185], v[116:119]
	v_mfma_f32_16x16x32_bf16 v[104:107], v[166:169], v[190:193], v[104:107]
	v_mfma_f32_16x16x32_bf16 v[100:103], v[174:177], v[190:193], v[100:103]
	v_mfma_f32_16x16x32_bf16 v[88:91], v[166:169], v[198:201], v[88:91]
	v_mfma_f32_16x16x32_bf16 v[84:87], v[174:177], v[198:201], v[84:87]
	v_mfma_f32_16x16x32_bf16 v[72:75], v[166:169], v[206:209], v[72:75]
	v_mfma_f32_16x16x32_bf16 v[68:71], v[174:177], v[206:209], v[68:71]
	v_mfma_f32_16x16x32_bf16 v[120:123], v[170:173], v[186:189], v[120:123]
	v_mfma_f32_16x16x32_bf16 v[116:119], v[178:181], v[186:189], v[116:119]
	v_mfma_f32_16x16x32_bf16 v[104:107], v[170:173], v[194:197], v[104:107]
	v_mfma_f32_16x16x32_bf16 v[100:103], v[178:181], v[194:197], v[100:103]
	v_mfma_f32_16x16x32_bf16 v[88:91], v[170:173], v[202:205], v[88:91]
	v_mfma_f32_16x16x32_bf16 v[84:87], v[178:181], v[202:205], v[84:87]
	v_mfma_f32_16x16x32_bf16 v[72:75], v[170:173], v[210:213], v[72:75]
	v_mfma_f32_16x16x32_bf16 v[68:71], v[178:181], v[210:213], v[68:71]
	s_barrier
	s_add_i32 s64, s65, s34
	v_lshl_add_u64 v[214:215], s[18:19], 0, v[2:3]
	s_mov_b32 m0, s64
	ds_read_b128 v[182:185], v149 offset:16384
	ds_read_b128 v[186:189], v149 offset:17408
	ds_read_b128 v[190:193], v149 offset:18432
	ds_read_b128 v[194:197], v149 offset:19456
	ds_read_b128 v[198:201], v149 offset:20480
	ds_read_b128 v[202:205], v149 offset:21504
	ds_read_b128 v[206:209], v149 offset:22528
	ds_read_b128 v[210:213], v149 offset:23552
	global_load_lds_dwordx4 v[214:215], off
	s_add_i32 m0, s64, 0x2000
	s_add_u32 s64, s18, 0xb0000
	v_lshl_add_u64 v[216:217], s[18:19], 0, v[136:137]
	s_addc_u32 s65, s19, 0
	s_add_i32 s63, s63, s34
	global_load_lds_dwordx4 v[216:217], off
	v_lshl_add_u64 v[218:219], s[64:65], 0, v[2:3]
	s_mov_b32 m0, s63
	v_lshl_add_u64 v[220:221], s[20:21], 0, v[134:135]
	global_load_lds_dwordx4 v[218:219], off
	v_lshl_add_u64 v[218:219], s[64:65], 0, v[136:137]
	s_add_i32 m0, s63, 0x2000
	s_nop 0
	global_load_lds_dwordx4 v[218:219], off
	v_lshl_add_u64 v[218:219], s[20:21], 0, v[132:133]
	s_mov_b32 m0, s35
	s_nop 0
	global_load_lds_dwordx4 v[218:219], off
	s_mov_b32 m0, s36
	s_nop 0
	global_load_lds_dwordx4 v[220:221], off
	s_waitcnt vmcnt(8)
	s_waitcnt lgkmcnt(0)
	s_barrier
; #define PG8_STAGE(bufoff, gbase, voff) do { _Pragma("unroll") for (int _i = 0; _i < 2; ++_i) \
;         __builtin_amdgcn_global_load_lds((const unsigned*)((const char*)(gbase) + (voff)[_i]), (PG8_LAS unsigned*)(lds + (bufoff) + ldsw + _i * 8192), 16, 0, 0); } while (0)
; #define PG8_LDA(dst, b, h) do { _Pragma("unroll") for (int m = 0; m < 4; ++m) _Pragma("unroll") for (int k = 0; k < 2; ++k) dst[m][k] = *(const PG8_LAS bf16x8*)(lds + PG8_SA(b, h) + aoff + m * 2048 + k * 1024); } while (0)
; #define PG8_LDB(dst, b, h) do { _Pragma("unroll") for (int n = 0; n < 2; ++n) _Pragma("unroll") for (int k = 0; k < 2; ++k) dst[n][k] = *(const PG8_LAS bf16x8*)(lds + PG8_SB(b, h) + boff + n * 2048 + k * 1024); } while (0)
; #define PG8_MMA(ai, bj, At, Bt) do { __builtin_amdgcn_s_setprio(1); _Pragma("unroll") for (int m = 0; m < 4; ++m) _Pragma("unroll") for (int n = 0; n < 2; ++n) _Pragma("unroll") for (int k = 0; k < 2; ++k) \
;         acc[ai][bj][m][n] = __builtin_amdgcn_mfma_f32_16x16x32_bf16(Bt[n][k], At[m][k], acc[ai][bj][m][n], 0, 0, 0); __builtin_amdgcn_s_setprio(0); } while (0)
; #define PG8_WAIT_V(n) asm volatile("s_waitcnt vmcnt(" #n ")" ::: "memory")
; #define PG8_WAIT_L(n) asm volatile("s_waitcnt lgkmcnt(" #n ")" ::: "memory")
; #define PG8_BAR __builtin_amdgcn_s_barrier()
; #define PG8_SCHED __builtin_amdgcn_sched_barrier(0)
; template <class Epi, class Sched, bool ALIGN_EPI = false, bool SP2 = false>
; __device__ __forceinline__ void gemm_phase(PG8_LAS unsigned char* lds, const Gemm g, const Sched& S, const Epi& E) {
;     ...
;             PG8_WAIT_V(8); PG8_WAIT_L(0); PG8_BAR; if (cur.half == 0) { PG8_MMA(1, 0, At, B0); PG8_MMA(1, 1, At, B1); } PG8_BAR; PG8_SCHED;
;             PG8_LDB(B0, 1, 0); PG8_LDB(B1, 1, 1); PG8_SCHED; PG8_LDA(At, 1, 0); PG8_STAGE(PG8_SA(0, 1), a2 + hstep, voffA);
;             PG8_WAIT_V(8); PG8_WAIT_L(0); PG8_BAR; PG8_MMA(0, 0, At, B0); PG8_MMA(0, 1, At, B1); PG8_BAR; PG8_SCHED;
	v_mfma_f32_16x16x32_bf16 v[64:67], v[150:153], v[182:185], v[64:67]
	v_mfma_f32_16x16x32_bf16 v[60:63], v[158:161], v[182:185], v[60:63]
	v_mfma_f32_16x16x32_bf16 v[48:51], v[150:153], v[190:193], v[48:51]
	v_mfma_f32_16x16x32_bf16 v[44:47], v[158:161], v[190:193], v[44:47]
	v_mfma_f32_16x16x32_bf16 v[32:35], v[150:153], v[198:201], v[32:35]
	v_mfma_f32_16x16x32_bf16 v[28:31], v[158:161], v[198:201], v[28:31]
	v_mfma_f32_16x16x32_bf16 v[16:19], v[150:153], v[206:209], v[16:19]
	v_mfma_f32_16x16x32_bf16 v[12:15], v[158:161], v[206:209], v[12:15]
	v_mfma_f32_16x16x32_bf16 v[64:67], v[154:157], v[186:189], v[64:67]
	v_mfma_f32_16x16x32_bf16 v[60:63], v[162:165], v[186:189], v[60:63]
	v_mfma_f32_16x16x32_bf16 v[48:51], v[154:157], v[194:197], v[48:51]
	v_mfma_f32_16x16x32_bf16 v[44:47], v[162:165], v[194:197], v[44:47]
	v_mfma_f32_16x16x32_bf16 v[32:35], v[154:157], v[202:205], v[32:35]
	v_mfma_f32_16x16x32_bf16 v[28:31], v[162:165], v[202:205], v[28:31]
	v_mfma_f32_16x16x32_bf16 v[16:19], v[154:157], v[210:213], v[16:19]
	v_mfma_f32_16x16x32_bf16 v[12:15], v[162:165], v[210:213], v[12:15]
	v_mfma_f32_16x16x32_bf16 v[56:59], v[166:169], v[182:185], v[56:59]
	v_mfma_f32_16x16x32_bf16 v[52:55], v[174:177], v[182:185], v[52:55]
	v_mfma_f32_16x16x32_bf16 v[40:43], v[166:169], v[190:193], v[40:43]
	v_mfma_f32_16x16x32_bf16 v[36:39], v[174:177], v[190:193], v[36:39]
	v_mfma_f32_16x16x32_bf16 v[24:27], v[166:169], v[198:201], v[24:27]
	v_mfma_f32_16x16x32_bf16 v[20:23], v[174:177], v[198:201], v[20:23]
	v_mfma_f32_16x16x32_bf16 v[8:11], v[166:169], v[206:209], v[8:11]
	v_mfma_f32_16x16x32_bf16 v[4:7], v[174:177], v[206:209], v[4:7]
	v_mfma_f32_16x16x32_bf16 v[56:59], v[170:173], v[186:189], v[56:59]
	v_mfma_f32_16x16x32_bf16 v[52:55], v[178:181], v[186:189], v[52:55]
	v_mfma_f32_16x16x32_bf16 v[40:43], v[170:173], v[194:197], v[40:43]
	v_mfma_f32_16x16x32_bf16 v[36:39], v[178:181], v[194:197], v[36:39]
	v_mfma_f32_16x16x32_bf16 v[24:27], v[170:173], v[202:205], v[24:27]
	v_mfma_f32_16x16x32_bf16 v[20:23], v[178:181], v[202:205], v[20:23]
	v_mfma_f32_16x16x32_bf16 v[8:11], v[170:173], v[210:213], v[8:11]
	v_mfma_f32_16x16x32_bf16 v[4:7], v[178:181], v[210:213], v[4:7]
	s_barrier
	s_add_i32 s63, 0, 0x18000
	s_add_i32 s64, 0, 0x1c000
	v_add_u32_e32 v162, s63, v148
	v_add_u32_e32 v178, s64, v148
	ds_read_b128 v[150:153], v162
	ds_read_b128 v[154:157], v162 offset:1024
	ds_read_b128 v[158:161], v162 offset:2048
	ds_read_b128 v[162:165], v162 offset:3072
	ds_read_b128 v[166:169], v178
	ds_read_b128 v[170:173], v178 offset:1024
	ds_read_b128 v[174:177], v178 offset:2048
	ds_read_b128 v[178:181], v178 offset:3072
	s_add_u32 s20, s20, 0xb0000
	s_addc_u32 s21, s21, 0
	s_mov_b32 m0, s38
	v_lshl_add_u64 v[230:231], s[20:21], 0, v[132:133]
	ds_read_b128 v[182:185], v149 offset:32768
	ds_read_b128 v[186:189], v149 offset:33792
	ds_read_b128 v[190:193], v149 offset:34816
	ds_read_b128 v[194:197], v149 offset:35840
	ds_read_b128 v[198:201], v149 offset:36864
	ds_read_b128 v[202:205], v149 offset:37888
	ds_read_b128 v[206:209], v149 offset:38912
	ds_read_b128 v[210:213], v149 offset:39936
	global_load_lds_dwordx4 v[230:231], off
	v_lshl_add_u64 v[230:231], s[20:21], 0, v[134:135]
	s_mov_b32 m0, s39
	s_nop 0
	global_load_lds_dwordx4 v[230:231], off
	s_waitcnt vmcnt(8)
	s_waitcnt lgkmcnt(0)
	s_barrier
	v_mfma_f32_16x16x32_bf16 v[128:131], v[150:153], v[182:185], v[128:131]
	v_mfma_f32_16x16x32_bf16 v[124:127], v[158:161], v[182:185], v[124:127]
	v_mfma_f32_16x16x32_bf16 v[112:115], v[150:153], v[190:193], v[112:115]
	v_mfma_f32_16x16x32_bf16 v[108:111], v[158:161], v[190:193], v[108:111]
	v_mfma_f32_16x16x32_bf16 v[96:99], v[150:153], v[198:201], v[96:99]
	v_mfma_f32_16x16x32_bf16 v[92:95], v[158:161], v[198:201], v[92:95]
	v_mfma_f32_16x16x32_bf16 v[80:83], v[150:153], v[206:209], v[80:83]
	v_mfma_f32_16x16x32_bf16 v[76:79], v[158:161], v[206:209], v[76:79]
	v_mfma_f32_16x16x32_bf16 v[128:131], v[154:157], v[186:189], v[128:131]
	v_mfma_f32_16x16x32_bf16 v[124:127], v[162:165], v[186:189], v[124:127]
	v_mfma_f32_16x16x32_bf16 v[112:115], v[154:157], v[194:197], v[112:115]
	v_mfma_f32_16x16x32_bf16 v[108:111], v[162:165], v[194:197], v[108:111]
	v_mfma_f32_16x16x32_bf16 v[96:99], v[154:157], v[202:205], v[96:99]
	v_mfma_f32_16x16x32_bf16 v[92:95], v[162:165], v[202:205], v[92:95]
	v_mfma_f32_16x16x32_bf16 v[80:83], v[154:157], v[210:213], v[80:83]
	v_mfma_f32_16x16x32_bf16 v[76:79], v[162:165], v[210:213], v[76:79]
	v_mfma_f32_16x16x32_bf16 v[120:123], v[166:169], v[182:185], v[120:123]
	v_mfma_f32_16x16x32_bf16 v[116:119], v[174:177], v[182:185], v[116:119]
	v_mfma_f32_16x16x32_bf16 v[104:107], v[166:169], v[190:193], v[104:107]
	v_mfma_f32_16x16x32_bf16 v[100:103], v[174:177], v[190:193], v[100:103]
	v_mfma_f32_16x16x32_bf16 v[88:91], v[166:169], v[198:201], v[88:91]
	v_mfma_f32_16x16x32_bf16 v[84:87], v[174:177], v[198:201], v[84:87]
	v_mfma_f32_16x16x32_bf16 v[72:75], v[166:169], v[206:209], v[72:75]
	v_mfma_f32_16x16x32_bf16 v[68:71], v[174:177], v[206:209], v[68:71]
	v_mfma_f32_16x16x32_bf16 v[120:123], v[170:173], v[186:189], v[120:123]
	v_mfma_f32_16x16x32_bf16 v[116:119], v[178:181], v[186:189], v[116:119]
	v_mfma_f32_16x16x32_bf16 v[104:107], v[170:173], v[194:197], v[104:107]
	v_mfma_f32_16x16x32_bf16 v[100:103], v[178:181], v[194:197], v[100:103]
	v_mfma_f32_16x16x32_bf16 v[88:91], v[170:173], v[202:205], v[88:91]
	v_mfma_f32_16x16x32_bf16 v[84:87], v[178:181], v[202:205], v[84:87]
	v_mfma_f32_16x16x32_bf16 v[72:75], v[170:173], v[210:213], v[72:75]
	v_mfma_f32_16x16x32_bf16 v[68:71], v[178:181], v[210:213], v[68:71]
	s_barrier
; #define PG8_STAGE(bufoff, gbase, voff) do { _Pragma("unroll") for (int _i = 0; _i < 2; ++_i) \
;         __builtin_amdgcn_global_load_lds((const unsigned*)((const char*)(gbase) + (voff)[_i]), (PG8_LAS unsigned*)(lds + (bufoff) + ldsw + _i * 8192), 16, 0, 0); } while (0)
; #define PG8_LDA(dst, b, h) do { _Pragma("unroll") for (int m = 0; m < 4; ++m) _Pragma("unroll") for (int k = 0; k < 2; ++k) dst[m][k] = *(const PG8_LAS bf16x8*)(lds + PG8_SA(b, h) + aoff + m * 2048 + k * 1024); } while (0)
; #define PG8_MMA(ai, bj, At, Bt) do { __builtin_amdgcn_s_setprio(1); _Pragma("unroll") for (int m = 0; m < 4; ++m) _Pragma("unroll") for (int n = 0; n < 2; ++n) _Pragma("unroll") for (int k = 0; k < 2; ++k) \
;         acc[ai][bj][m][n] = __builtin_amdgcn_mfma_f32_16x16x32_bf16(Bt[n][k], At[m][k], acc[ai][bj][m][n], 0, 0, 0); __builtin_amdgcn_s_setprio(0); } while (0)
; #define PG8_WAIT_V(n) asm volatile("s_waitcnt vmcnt(" #n ")" ::: "memory")
; #define PG8_WAIT_L(n) asm volatile("s_waitcnt lgkmcnt(" #n ")" ::: "memory")
; #define PG8_BAR __builtin_amdgcn_s_barrier()
; #define PG8_SCHED __builtin_amdgcn_sched_barrier(0)
; template <class Epi, class Sched, bool ALIGN_EPI = false, bool SP2 = false>
; __device__ __forceinline__ void gemm_phase(PG8_LAS unsigned char* lds, const Gemm g, const Sched& S, const Epi& E) {
;     ...
;             PG8_LDA(At, 1, 1); PG8_STAGE(PG8_SB(1, 0), b3, voffB); PG8_STAGE(PG8_SB(1, 1), b3 + hstep, voffB); PG8_STAGE(PG8_SA(1, 0), a3, voffA);
;             PG8_WAIT_V(8); PG8_WAIT_L(0); PG8_BAR; if (cur.half == 0) { PG8_MMA(1, 0, At, B0); PG8_MMA(1, 1, At, B1); } PG8_BAR; PG8_SCHED;
;     ...
;         if (!has_next) break;
;         if constexpr (!Epi::CHAIN) {
; #pragma unroll
;         for (int a = 0; a < 2; ++a)
; #pragma unroll
;             for (int b = 0; b < 2; ++b)
; #pragma unroll
;                 for (int m = 0; m < 4; ++m)
; #pragma unroll
;                     for (int n = 0; n < 2; ++n) acc[a][b][m][n] = (f32x4){0.f, 0.f, 0.f, 0.f};
;         }
;         cur = nxt; cA = nA; cB = nB; ++ui;
	s_add_i32 s20, s63, s34
	v_lshl_add_u64 v[214:215], v[214:215], 0, s[42:43]
	s_mov_b32 m0, s20
	ds_read_b128 v[182:185], v149 offset:49152
	ds_read_b128 v[186:189], v149 offset:50176
	ds_read_b128 v[190:193], v149 offset:51200
	ds_read_b128 v[194:197], v149 offset:52224
	ds_read_b128 v[198:201], v149 offset:53248
	ds_read_b128 v[202:205], v149 offset:54272
	ds_read_b128 v[206:209], v149 offset:55296
	ds_read_b128 v[210:213], v149 offset:56320
	global_load_lds_dwordx4 v[214:215], off
	s_add_i32 m0, s20, 0x2000
	s_add_u32 s18, s18, 0xb0080
	v_lshl_add_u64 v[214:215], v[216:217], 0, s[42:43]
	s_addc_u32 s19, s19, 0
	s_add_i32 s20, s64, s34
	global_load_lds_dwordx4 v[214:215], off
	v_lshl_add_u64 v[214:215], s[18:19], 0, v[2:3]
	s_mov_b32 m0, s20
	s_nop 0
	global_load_lds_dwordx4 v[214:215], off
	v_lshl_add_u64 v[214:215], s[18:19], 0, v[136:137]
	s_add_i32 m0, s20, 0x2000
	s_nop 0
	global_load_lds_dwordx4 v[214:215], off
	v_lshl_add_u64 v[214:215], v[218:219], 0, s[42:43]
	s_mov_b32 m0, s40
	s_nop 0
	global_load_lds_dwordx4 v[214:215], off
	v_lshl_add_u64 v[214:215], v[220:221], 0, s[42:43]
	s_mov_b32 m0, s41
	s_nop 0
	global_load_lds_dwordx4 v[214:215], off
	s_waitcnt vmcnt(8)
	s_waitcnt lgkmcnt(0)
	s_barrier
	v_mfma_f32_16x16x32_bf16 v[64:67], v[150:153], v[182:185], v[64:67]
	v_mfma_f32_16x16x32_bf16 v[60:63], v[158:161], v[182:185], v[60:63]
	v_mfma_f32_16x16x32_bf16 v[48:51], v[150:153], v[190:193], v[48:51]
	v_mfma_f32_16x16x32_bf16 v[44:47], v[158:161], v[190:193], v[44:47]
	v_mfma_f32_16x16x32_bf16 v[32:35], v[150:153], v[198:201], v[32:35]
	v_mfma_f32_16x16x32_bf16 v[28:31], v[158:161], v[198:201], v[28:31]
	v_mfma_f32_16x16x32_bf16 v[16:19], v[150:153], v[206:209], v[16:19]
	v_mfma_f32_16x16x32_bf16 v[12:15], v[158:161], v[206:209], v[12:15]
	v_mfma_f32_16x16x32_bf16 v[64:67], v[154:157], v[186:189], v[64:67]
	v_mfma_f32_16x16x32_bf16 v[60:63], v[162:165], v[186:189], v[60:63]
	v_mfma_f32_16x16x32_bf16 v[48:51], v[154:157], v[194:197], v[48:51]
	v_mfma_f32_16x16x32_bf16 v[44:47], v[162:165], v[194:197], v[44:47]
	v_mfma_f32_16x16x32_bf16 v[32:35], v[154:157], v[202:205], v[32:35]
	v_mfma_f32_16x16x32_bf16 v[28:31], v[162:165], v[202:205], v[28:31]
	v_mfma_f32_16x16x32_bf16 v[16:19], v[154:157], v[210:213], v[16:19]
	v_mfma_f32_16x16x32_bf16 v[12:15], v[162:165], v[210:213], v[12:15]
	v_mfma_f32_16x16x32_bf16 v[56:59], v[166:169], v[182:185], v[56:59]
	v_mfma_f32_16x16x32_bf16 v[52:55], v[174:177], v[182:185], v[52:55]
	v_mfma_f32_16x16x32_bf16 v[40:43], v[166:169], v[190:193], v[40:43]
	v_mfma_f32_16x16x32_bf16 v[36:39], v[174:177], v[190:193], v[36:39]
	v_mfma_f32_16x16x32_bf16 v[24:27], v[166:169], v[198:201], v[24:27]
	v_mfma_f32_16x16x32_bf16 v[20:23], v[174:177], v[198:201], v[20:23]
	v_mfma_f32_16x16x32_bf16 v[8:11], v[166:169], v[206:209], v[8:11]
	v_mfma_f32_16x16x32_bf16 v[4:7], v[174:177], v[206:209], v[4:7]
	v_mfma_f32_16x16x32_bf16 v[56:59], v[170:173], v[186:189], v[56:59]
	v_mfma_f32_16x16x32_bf16 v[52:55], v[178:181], v[186:189], v[52:55]
	v_mfma_f32_16x16x32_bf16 v[40:43], v[170:173], v[194:197], v[40:43]
	v_mfma_f32_16x16x32_bf16 v[36:39], v[178:181], v[194:197], v[36:39]
	v_mfma_f32_16x16x32_bf16 v[24:27], v[170:173], v[202:205], v[24:27]
	v_mfma_f32_16x16x32_bf16 v[20:23], v[178:181], v[202:205], v[20:23]
	v_mfma_f32_16x16x32_bf16 v[8:11], v[170:173], v[210:213], v[8:11]
	v_mfma_f32_16x16x32_bf16 v[4:7], v[178:181], v[210:213], v[4:7]
	s_barrier
	s_add_i32 s62, s62, 2
	s_add_u32 s0, s0, 0x100
	s_addc_u32 s1, s1, 0
	s_cmp_gt_u32 s62, 41
	s_cbranch_scc0 .LBB0_1780
	s_add_u32 s0, s60, 0xffffff00
	s_addc_u32 s1, s61, -1
	s_and_b64 vcc, exec, s[4:5]
	s_cbranch_vccnz .LBB0_1783
	v_mov_b32_e32 v4, 0
	s_mov_b32 s16, s58
	s_mov_b32 s23, s57
	s_mov_b64 s[6:7], s[14:15]
	s_mov_b32 s56, s59
	v_mov_b32_e32 v5, v4
	v_mov_b32_e32 v6, v4
	v_mov_b32_e32 v7, v4
	v_mov_b32_e32 v8, v4
	v_mov_b32_e32 v9, v4
	v_mov_b32_e32 v10, v4
	v_mov_b32_e32 v11, v4
	v_mov_b32_e32 v20, v4
	v_mov_b32_e32 v21, v4
	v_mov_b32_e32 v22, v4
	v_mov_b32_e32 v23, v4
	v_mov_b32_e32 v24, v4
	v_mov_b32_e32 v25, v4
	v_mov_b32_e32 v26, v4
	v_mov_b32_e32 v27, v4
	v_mov_b32_e32 v36, v4
	v_mov_b32_e32 v37, v4
	v_mov_b32_e32 v38, v4
	v_mov_b32_e32 v39, v4
	v_mov_b32_e32 v40, v4
	v_mov_b32_e32 v41, v4
	v_mov_b32_e32 v42, v4
	v_mov_b32_e32 v43, v4
	v_mov_b32_e32 v52, v4
	v_mov_b32_e32 v53, v4
	v_mov_b32_e32 v54, v4
	v_mov_b32_e32 v55, v4
	v_mov_b32_e32 v56, v4
	v_mov_b32_e32 v57, v4
	v_mov_b32_e32 v58, v4
	v_mov_b32_e32 v59, v4
	v_mov_b32_e32 v12, v4
	v_mov_b32_e32 v13, v4
	v_mov_b32_e32 v14, v4
	v_mov_b32_e32 v15, v4
	v_mov_b32_e32 v16, v4
	v_mov_b32_e32 v17, v4
	v_mov_b32_e32 v18, v4
	v_mov_b32_e32 v19, v4
	v_mov_b32_e32 v28, v4
	v_mov_b32_e32 v29, v4
	v_mov_b32_e32 v30, v4
	v_mov_b32_e32 v31, v4
	v_mov_b32_e32 v32, v4
	v_mov_b32_e32 v33, v4
	v_mov_b32_e32 v34, v4
	v_mov_b32_e32 v35, v4
	v_mov_b32_e32 v44, v4
	v_mov_b32_e32 v45, v4
	v_mov_b32_e32 v46, v4
	v_mov_b32_e32 v47, v4
	v_mov_b32_e32 v48, v4
	v_mov_b32_e32 v49, v4
	v_mov_b32_e32 v50, v4
	v_mov_b32_e32 v51, v4
	v_mov_b32_e32 v60, v4
	v_mov_b32_e32 v61, v4
	v_mov_b32_e32 v62, v4
	v_mov_b32_e32 v63, v4
	v_mov_b32_e32 v64, v4
	v_mov_b32_e32 v65, v4
	v_mov_b32_e32 v66, v4
	v_mov_b32_e32 v67, v4
	v_mov_b32_e32 v68, v4
	v_mov_b32_e32 v69, v4
	v_mov_b32_e32 v70, v4
	v_mov_b32_e32 v71, v4
	v_mov_b32_e32 v72, v4
	v_mov_b32_e32 v73, v4
	v_mov_b32_e32 v74, v4
	v_mov_b32_e32 v75, v4
	v_mov_b32_e32 v84, v4
	v_mov_b32_e32 v85, v4
	v_mov_b32_e32 v86, v4
	v_mov_b32_e32 v87, v4
	v_mov_b32_e32 v88, v4
	v_mov_b32_e32 v89, v4
	v_mov_b32_e32 v90, v4
	v_mov_b32_e32 v91, v4
	v_mov_b32_e32 v100, v4
	v_mov_b32_e32 v101, v4
	v_mov_b32_e32 v102, v4
	v_mov_b32_e32 v103, v4
	v_mov_b32_e32 v104, v4
	v_mov_b32_e32 v105, v4
	v_mov_b32_e32 v106, v4
	v_mov_b32_e32 v107, v4
	v_mov_b32_e32 v116, v4
	v_mov_b32_e32 v117, v4
	v_mov_b32_e32 v118, v4
	v_mov_b32_e32 v119, v4
	v_mov_b32_e32 v120, v4
	v_mov_b32_e32 v121, v4
	v_mov_b32_e32 v122, v4
	v_mov_b32_e32 v123, v4
	v_mov_b32_e32 v76, v4
	v_mov_b32_e32 v77, v4
	v_mov_b32_e32 v78, v4
	v_mov_b32_e32 v79, v4
	v_mov_b32_e32 v80, v4
	v_mov_b32_e32 v81, v4
	v_mov_b32_e32 v82, v4
	v_mov_b32_e32 v83, v4
	v_mov_b32_e32 v92, v4
	v_mov_b32_e32 v93, v4
	v_mov_b32_e32 v94, v4
	v_mov_b32_e32 v95, v4
	v_mov_b32_e32 v96, v4
	v_mov_b32_e32 v97, v4
	v_mov_b32_e32 v98, v4
	v_mov_b32_e32 v99, v4
	v_mov_b32_e32 v108, v4
	v_mov_b32_e32 v109, v4
	v_mov_b32_e32 v110, v4
	v_mov_b32_e32 v111, v4
	v_mov_b32_e32 v112, v4
	v_mov_b32_e32 v113, v4
	v_mov_b32_e32 v114, v4
	v_mov_b32_e32 v115, v4
	v_mov_b32_e32 v124, v4
	v_mov_b32_e32 v125, v4
	v_mov_b32_e32 v126, v4
	v_mov_b32_e32 v127, v4
	v_mov_b32_e32 v128, v4
	v_mov_b32_e32 v129, v4
	v_mov_b32_e32 v130, v4
	v_mov_b32_e32 v131, v4
	s_andn2_b64 vcc, exec, s[8:9]
	s_cbranch_vccnz .LBB0_1784
	s_branch .LBB0_1785
